# speedup vs baseline: 1.0712x; 1.0712x over previous
.LBB0_3:
	s_cmpk_gt_u32 s2, 0x27f
	s_cbranch_scc0 .LBB0_46
	s_cmpk_gt_u32 s2, 0x29f
	s_cbranch_scc0 .LBB0_12
	s_add_i32 s4, s2, 0xfffffd60
	s_cmpk_gt_u32 s4, 0x3ff
	s_cbranch_scc1 .LBB0_2
	s_lshl_b32 s4, s4, 2
	s_load_dwordx2 s[8:9], s[0:1], 0x0
	s_load_dwordx2 s[6:7], s[0:1], 0x8
	s_load_dwordx2 s[12:13], s[0:1], 0x40
	s_load_dwordx4 s[16:19], s[0:1], 0x48
	v_lshlrev_b32_e32 v1, 5, v0
	s_lshl_b32 s10, s4, 13
	v_add_u32_e32 v2, 0x2000, v1
	v_add_u32_e32 v3, 0x4000, v1
	v_add_u32_e32 v4, 0x6000, v1
	s_waitcnt lgkmcnt(0)
	s_add_u32 s8, s8, s10
	s_addc_u32 s9, s9, 0
	v_cmp_gt_u32_e32 vcc, 4, v0
	s_and_saveexec_b64 s[14:15], vcc
	s_cbranch_execz .Lx_nozero
	v_mov_b32_e32 v10, 0
	v_mov_b32_e32 v11, 0
	v_lshlrev_b32_e32 v7, 3, v0
	s_lshl_b32 s10, s4, 3
	s_add_u32 s12, s12, s10
	s_addc_u32 s13, s13, 0
	v_lshlrev_b32_e32 v9, 2, v0
	s_lshl_b32 s10, s4, 2
	s_add_u32 s18, s18, s10
	s_addc_u32 s19, s19, 0
	global_store_dwordx2 v7, v[10:11], s[12:13]
	global_store_dword v9, v10, s[18:19]
	s_cmp_lg_u32 s4, 0
	s_cbranch_scc1 .Lx_nozero
	global_store_dword v10, v10, s[16:17]
.Lx_nozero:
	s_or_b64 exec, exec, s[14:15]
	global_load_dwordx4 v[16:19], v1, s[8:9] nt
	global_load_dwordx4 v[20:23], v1, s[8:9] offset:16 nt
	global_load_dwordx4 v[24:27], v2, s[8:9] nt
	global_load_dwordx4 v[28:31], v2, s[8:9] offset:16 nt
	global_load_dwordx4 v[32:35], v3, s[8:9] nt
	global_load_dwordx4 v[36:39], v3, s[8:9] offset:16 nt
	global_load_dwordx4 v[40:43], v4, s[8:9] nt
	global_load_dwordx4 v[44:47], v4, s[8:9] offset:16 nt
	s_lshr_b32 s10, s4, 7
	s_lshl_b32 s10, s10, 19
	s_and_b32 s11, s4, 0x7f
	s_lshl_b32 s11, s11, 7
	s_add_u32 s10, s10, s11
	s_add_u32 s6, s6, s10
	s_addc_u32 s7, s7, 0
	v_lshrrev_b32_e32 v8, 3, v0
	v_and_b32_e32 v9, 7, v0
	v_lshlrev_b32_e32 v8, 14, v8
	v_lshl_or_b32 v8, v9, 4, v8
	s_mov_b32 s20, 0x42000000
	s_mov_b32 s21, 0x42000000
	s_waitcnt vmcnt(6)
	v_pk_mul_f32 v[16:17], v[16:17], s[20:21] op_sel_hi:[1,0]
	v_pk_mul_f32 v[18:19], v[18:19], s[20:21] op_sel_hi:[1,0]
	v_pk_mul_f32 v[20:21], v[20:21], s[20:21] op_sel_hi:[1,0]
	v_pk_mul_f32 v[22:23], v[22:23], s[20:21] op_sel_hi:[1,0]
	v_cvt_pk_f16_f32 v16, v16, v17
	v_cvt_pk_f16_f32 v17, v18, v19
	v_cvt_pk_f16_f32 v18, v20, v21
	v_cvt_pk_f16_f32 v19, v22, v23
	global_store_dwordx4 v8, v[16:19], s[6:7]
	s_waitcnt vmcnt(5)
	v_pk_mul_f32 v[24:25], v[24:25], s[20:21] op_sel_hi:[1,0]
	v_pk_mul_f32 v[26:27], v[26:27], s[20:21] op_sel_hi:[1,0]
	v_pk_mul_f32 v[28:29], v[28:29], s[20:21] op_sel_hi:[1,0]
	v_pk_mul_f32 v[30:31], v[30:31], s[20:21] op_sel_hi:[1,0]
	v_cvt_pk_f16_f32 v24, v24, v25
	v_cvt_pk_f16_f32 v25, v26, v27
	v_cvt_pk_f16_f32 v26, v28, v29
	v_cvt_pk_f16_f32 v27, v30, v31
	global_store_dwordx4 v8, v[24:27], s[6:7] offset:128
	s_waitcnt vmcnt(4)
	v_pk_mul_f32 v[32:33], v[32:33], s[20:21] op_sel_hi:[1,0]
	v_pk_mul_f32 v[34:35], v[34:35], s[20:21] op_sel_hi:[1,0]
	v_pk_mul_f32 v[36:37], v[36:37], s[20:21] op_sel_hi:[1,0]
	v_pk_mul_f32 v[38:39], v[38:39], s[20:21] op_sel_hi:[1,0]
	v_cvt_pk_f16_f32 v32, v32, v33
	v_cvt_pk_f16_f32 v33, v34, v35
	v_cvt_pk_f16_f32 v34, v36, v37
	v_cvt_pk_f16_f32 v35, v38, v39
	global_store_dwordx4 v8, v[32:35], s[6:7] offset:256
	s_waitcnt vmcnt(3)
	v_pk_mul_f32 v[40:41], v[40:41], s[20:21] op_sel_hi:[1,0]
	v_pk_mul_f32 v[42:43], v[42:43], s[20:21] op_sel_hi:[1,0]
	v_pk_mul_f32 v[44:45], v[44:45], s[20:21] op_sel_hi:[1,0]
	v_pk_mul_f32 v[46:47], v[46:47], s[20:21] op_sel_hi:[1,0]
	v_cvt_pk_f16_f32 v40, v40, v41
	v_cvt_pk_f16_f32 v41, v42, v43
	v_cvt_pk_f16_f32 v42, v44, v45
	v_cvt_pk_f16_f32 v43, v46, v47
	global_store_dwordx4 v8, v[40:43], s[6:7] offset:384
	s_endpgm
.LBB0_12:
	s_and_b64 vcc, exec, s[4:5]
	s_cbranch_vccz .LBB0_114
	s_load_dwordx2 s[4:5], s[0:1], 0x20
	s_load_dwordx2 s[6:7], s[0:1], 0x38
	s_lshl_b32 s8, s2, 3
	s_and_b32 s8, s8, 0x1fc0
	s_addk_i32 s8, 0xec00
	s_lshl_b32 s3, s2, 6
	s_and_b32 s3, s3, 0x1c0
	v_and_b32_e32 v6, 63, v0
	v_lshrrev_b32_e32 v1, 6, v0
	v_or_b32_e32 v4, s8, v6
	s_movk_i32 s9, 0xc8
	v_cmp_gt_u32_e32 vcc, 0xc8, v4
	v_min_u32_e32 v5, 0xc7, v4
	v_add_u32_e32 v7, s3, v1
	s_mov_b64 s[10:11], vcc
	v_mul_u32_u24_e32 v9, 0x104, v1
	v_lshl_add_u32 v9, v6, 2, v9
	s_waitcnt lgkmcnt(0)
	v_add_u32_e32 v8, 0, v7
	v_min_u32_e32 v8, 0x1f3, v8
	v_mad_u32_u24 v8, v8, s9, v5
	v_lshlrev_b32_e32 v8, 2, v8
	global_load_dword v16, v8, s[4:5]
	v_add_u32_e32 v8, 4, v7
	v_min_u32_e32 v8, 0x1f3, v8
	v_mad_u32_u24 v8, v8, s9, v5
	v_lshlrev_b32_e32 v8, 2, v8
	global_load_dword v17, v8, s[4:5]
	v_add_u32_e32 v8, 8, v7
	v_min_u32_e32 v8, 0x1f3, v8
	v_mad_u32_u24 v8, v8, s9, v5
	v_lshlrev_b32_e32 v8, 2, v8
	global_load_dword v18, v8, s[4:5]
	v_add_u32_e32 v8, 12, v7
	v_min_u32_e32 v8, 0x1f3, v8
	v_mad_u32_u24 v8, v8, s9, v5
	v_lshlrev_b32_e32 v8, 2, v8
	global_load_dword v19, v8, s[4:5]
	v_add_u32_e32 v8, 16, v7
	v_min_u32_e32 v8, 0x1f3, v8
	v_mad_u32_u24 v8, v8, s9, v5
	v_lshlrev_b32_e32 v8, 2, v8
	global_load_dword v20, v8, s[4:5]
	v_add_u32_e32 v8, 20, v7
	v_min_u32_e32 v8, 0x1f3, v8
	v_mad_u32_u24 v8, v8, s9, v5
	v_lshlrev_b32_e32 v8, 2, v8
	global_load_dword v21, v8, s[4:5]
	v_add_u32_e32 v8, 24, v7
	v_min_u32_e32 v8, 0x1f3, v8
	v_mad_u32_u24 v8, v8, s9, v5
	v_lshlrev_b32_e32 v8, 2, v8
	global_load_dword v22, v8, s[4:5]
	v_add_u32_e32 v8, 28, v7
	v_min_u32_e32 v8, 0x1f3, v8
	v_mad_u32_u24 v8, v8, s9, v5
	v_lshlrev_b32_e32 v8, 2, v8
	global_load_dword v23, v8, s[4:5]
	v_add_u32_e32 v8, 32, v7
	v_min_u32_e32 v8, 0x1f3, v8
	v_mad_u32_u24 v8, v8, s9, v5
	v_lshlrev_b32_e32 v8, 2, v8
	global_load_dword v24, v8, s[4:5]
	v_add_u32_e32 v8, 36, v7
	v_min_u32_e32 v8, 0x1f3, v8
	v_mad_u32_u24 v8, v8, s9, v5
	v_lshlrev_b32_e32 v8, 2, v8
	global_load_dword v25, v8, s[4:5]
	v_add_u32_e32 v8, 40, v7
	v_min_u32_e32 v8, 0x1f3, v8
	v_mad_u32_u24 v8, v8, s9, v5
	v_lshlrev_b32_e32 v8, 2, v8
	global_load_dword v26, v8, s[4:5]
	v_add_u32_e32 v8, 44, v7
	v_min_u32_e32 v8, 0x1f3, v8
	v_mad_u32_u24 v8, v8, s9, v5
	v_lshlrev_b32_e32 v8, 2, v8
	global_load_dword v27, v8, s[4:5]
	v_add_u32_e32 v8, 48, v7
	v_min_u32_e32 v8, 0x1f3, v8
	v_mad_u32_u24 v8, v8, s9, v5
	v_lshlrev_b32_e32 v8, 2, v8
	global_load_dword v28, v8, s[4:5]
	v_add_u32_e32 v8, 52, v7
	v_min_u32_e32 v8, 0x1f3, v8
	v_mad_u32_u24 v8, v8, s9, v5
	v_lshlrev_b32_e32 v8, 2, v8
	global_load_dword v29, v8, s[4:5]
	v_add_u32_e32 v8, 56, v7
	v_min_u32_e32 v8, 0x1f3, v8
	v_mad_u32_u24 v8, v8, s9, v5
	v_lshlrev_b32_e32 v8, 2, v8
	global_load_dword v30, v8, s[4:5]
	v_add_u32_e32 v8, 60, v7
	v_min_u32_e32 v8, 0x1f3, v8
	v_mad_u32_u24 v8, v8, s9, v5
	v_lshlrev_b32_e32 v8, 2, v8
	global_load_dword v31, v8, s[4:5]
	v_cmp_gt_u32_e32 vcc, 0x1f4, v7
	s_and_b64 vcc, vcc, s[10:11]
	s_waitcnt vmcnt(15)
	v_cndmask_b32_e32 v16, 0, v16, vcc
	ds_write_b32 v9, v16
	v_cmp_gt_u32_e32 vcc, 0x1f0, v7
	s_and_b64 vcc, vcc, s[10:11]
	s_waitcnt vmcnt(14)
	v_cndmask_b32_e32 v17, 0, v17, vcc
	ds_write_b32 v9, v17 offset:1040
	v_cmp_gt_u32_e32 vcc, 0x1ec, v7
	s_and_b64 vcc, vcc, s[10:11]
	s_waitcnt vmcnt(13)
	v_cndmask_b32_e32 v18, 0, v18, vcc
	ds_write_b32 v9, v18 offset:2080
	v_cmp_gt_u32_e32 vcc, 0x1e8, v7
	s_and_b64 vcc, vcc, s[10:11]
	s_waitcnt vmcnt(12)
	v_cndmask_b32_e32 v19, 0, v19, vcc
	ds_write_b32 v9, v19 offset:3120
	v_cmp_gt_u32_e32 vcc, 0x1e4, v7
	s_and_b64 vcc, vcc, s[10:11]
	s_waitcnt vmcnt(11)
	v_cndmask_b32_e32 v20, 0, v20, vcc
	ds_write_b32 v9, v20 offset:4160
	v_cmp_gt_u32_e32 vcc, 0x1e0, v7
	s_and_b64 vcc, vcc, s[10:11]
	s_waitcnt vmcnt(10)
	v_cndmask_b32_e32 v21, 0, v21, vcc
	ds_write_b32 v9, v21 offset:5200
	v_cmp_gt_u32_e32 vcc, 0x1dc, v7
	s_and_b64 vcc, vcc, s[10:11]
	s_waitcnt vmcnt(9)
	v_cndmask_b32_e32 v22, 0, v22, vcc
	ds_write_b32 v9, v22 offset:6240
	v_cmp_gt_u32_e32 vcc, 0x1d8, v7
	s_and_b64 vcc, vcc, s[10:11]
	s_waitcnt vmcnt(8)
	v_cndmask_b32_e32 v23, 0, v23, vcc
	ds_write_b32 v9, v23 offset:7280
	v_cmp_gt_u32_e32 vcc, 0x1d4, v7
	s_and_b64 vcc, vcc, s[10:11]
	s_waitcnt vmcnt(7)
	v_cndmask_b32_e32 v24, 0, v24, vcc
	ds_write_b32 v9, v24 offset:8320
	v_cmp_gt_u32_e32 vcc, 0x1d0, v7
	s_and_b64 vcc, vcc, s[10:11]
	s_waitcnt vmcnt(6)
	v_cndmask_b32_e32 v25, 0, v25, vcc
	ds_write_b32 v9, v25 offset:9360
	v_cmp_gt_u32_e32 vcc, 0x1cc, v7
	s_and_b64 vcc, vcc, s[10:11]
	s_waitcnt vmcnt(5)
	v_cndmask_b32_e32 v26, 0, v26, vcc
	ds_write_b32 v9, v26 offset:10400
	v_cmp_gt_u32_e32 vcc, 0x1c8, v7
	s_and_b64 vcc, vcc, s[10:11]
	s_waitcnt vmcnt(4)
	v_cndmask_b32_e32 v27, 0, v27, vcc
	ds_write_b32 v9, v27 offset:11440
	v_cmp_gt_u32_e32 vcc, 0x1c4, v7
	s_and_b64 vcc, vcc, s[10:11]
	s_waitcnt vmcnt(3)
	v_cndmask_b32_e32 v28, 0, v28, vcc
	ds_write_b32 v9, v28 offset:12480
	v_cmp_gt_u32_e32 vcc, 0x1c0, v7
	s_and_b64 vcc, vcc, s[10:11]
	s_waitcnt vmcnt(2)
	v_cndmask_b32_e32 v29, 0, v29, vcc
	ds_write_b32 v9, v29 offset:13520
	v_cmp_gt_u32_e32 vcc, 0x1bc, v7
	s_and_b64 vcc, vcc, s[10:11]
	s_waitcnt vmcnt(1)
	v_cndmask_b32_e32 v30, 0, v30, vcc
	ds_write_b32 v9, v30 offset:14560
	v_cmp_gt_u32_e32 vcc, 0x1b8, v7
	s_and_b64 vcc, vcc, s[10:11]
	s_waitcnt vmcnt(0)
	v_cndmask_b32_e32 v31, 0, v31, vcc
	ds_write_b32 v9, v31 offset:15600
	v_lshrrev_b32_e32 v1, 2, v0
	v_and_b32_e32 v12, 3, v0
	v_and_b32_e32 v2, 0xfc, v0
	s_movk_i32 s4, 0x820
	v_add_u32_e32 v6, s8, v1
	v_mad_u32_u24 v1, v12, s4, v2
	s_waitcnt lgkmcnt(0)
	s_barrier
	ds_read2_b32 v[2:3], v1 offset1:65
	ds_read2_b32 v[10:11], v1 offset0:130 offset1:195
	v_mov_b32_e32 v7, 0
	v_lshlrev_b64 v[4:5], 10, v[6:7]
	s_mov_b32 s4, 0x45000000
	v_lshl_add_u64 v[8:9], s[6:7], 0, v[4:5]
	s_waitcnt lgkmcnt(1)
	v_fma_mixlo_f16 v4, v2, s4, 0
	v_mov_b32_e32 v2, v3
	s_waitcnt lgkmcnt(0)
	v_mov_b32_e32 v3, v10
	v_add_u32_e32 v6, 0x400, v1
	ds_read2_b32 v[14:15], v6 offset0:4 offset1:69
	v_pk_mul_f32 v[2:3], v[2:3], s[4:5] op_sel_hi:[1,0]
	s_waitcnt lgkmcnt(0)
	v_mov_b32_e32 v5, v14
	v_cvt_pk_f16_f32 v3, v2, v3
	v_pack_b32_f16 v2, v4, v3
	v_mov_b32_e32 v4, v11
	ds_read2_b32 v[10:11], v6 offset0:134 offset1:199
	v_pk_mul_f32 v[4:5], v[4:5], s[4:5] op_sel_hi:[1,0]
	s_nop 0
	v_cvt_pk_f16_f32 v6, v4, v5
	v_mov_b32_e32 v4, v15
	s_waitcnt lgkmcnt(0)
	v_mov_b32_e32 v5, v10
	v_pk_mul_f32 v[4:5], v[4:5], s[4:5] op_sel_hi:[1,0]
	v_alignbit_b32 v3, v6, v3, 16
	v_cvt_pk_f16_f32 v5, v4, v5
	v_alignbit_b32 v4, v5, v6, 16
	v_lshlrev_b32_e32 v6, 4, v12
	v_lshrrev_b32_e32 v5, 16, v5
	v_lshl_or_b32 v6, s3, 1, v6
	v_fma_mixhi_f16 v5, v11, s4, 0
	v_lshl_add_u64 v[10:11], v[8:9], 0, v[6:7]
	global_store_dwordx4 v[10:11], v[2:5], off
	v_or_b32_e32 v6, 64, v6
	v_lshl_add_u64 v[6:7], v[8:9], 0, v[6:7]
	v_add_u32_e32 v4, 0x2000, v1
	ds_read2_b32 v[2:3], v4 offset0:32 offset1:97
	ds_read2_b32 v[4:5], v4 offset0:162 offset1:227
	v_add_u32_e32 v1, 0x2400, v1
	ds_read2_b32 v[12:13], v1 offset0:36 offset1:101
	ds_read2_b32 v[10:11], v1 offset0:166 offset1:231
	s_waitcnt lgkmcnt(3)
	v_fma_mixlo_f16 v1, v2, s4, 0
	v_mov_b32_e32 v2, v3
	s_waitcnt lgkmcnt(2)
	v_mov_b32_e32 v3, v4
	v_pk_mul_f32 v[2:3], v[2:3], s[4:5] op_sel_hi:[1,0]
	v_mov_b32_e32 v4, v5
	s_waitcnt lgkmcnt(1)
	v_mov_b32_e32 v5, v12
	v_cvt_pk_f16_f32 v3, v2, v3
	v_pk_mul_f32 v[4:5], v[4:5], s[4:5] op_sel_hi:[1,0]
	v_pack_b32_f16 v2, v1, v3
	v_cvt_pk_f16_f32 v1, v4, v5
	v_mov_b32_e32 v4, v13
	s_waitcnt lgkmcnt(0)
	v_mov_b32_e32 v5, v10
	v_pk_mul_f32 v[4:5], v[4:5], s[4:5] op_sel_hi:[1,0]
	v_alignbit_b32 v3, v1, v3, 16
	v_cvt_pk_f16_f32 v5, v4, v5
	v_alignbit_b32 v4, v5, v1, 16
	v_lshrrev_b32_e32 v5, 16, v5
	v_fma_mixhi_f16 v5, v11, s4, 0
	global_store_dwordx4 v[6:7], v[2:5], off
	s_mov_b64 s[4:5], 0

.LBB0_47:
	s_load_dwordx2 s[4:5], s[0:1], 0x18
	s_load_dwordx2 s[6:7], s[0:1], 0x30
	s_lshl_b32 s8, s2, 2
	s_and_b32 s8, s8, 0xfc0
	s_addk_i32 s8, 0xf800
	s_lshl_b32 s3, s2, 6
	s_and_b32 s3, s3, 0x3c0
	v_and_b32_e32 v6, 63, v0
	v_lshrrev_b32_e32 v1, 6, v0
	v_or_b32_e32 v4, s8, v6
	s_movk_i32 s9, 0x1f4
	v_cmp_gt_u32_e32 vcc, 0x1f4, v4
	v_min_u32_e32 v5, 0x1f3, v4
	v_add_u32_e32 v7, s3, v1
	s_mov_b64 s[10:11], vcc
	v_mul_u32_u24_e32 v9, 0x104, v1
	v_lshl_add_u32 v9, v6, 2, v9
	s_waitcnt lgkmcnt(0)
	v_add_u32_e32 v8, 0, v7
	v_min_u32_e32 v8, 0x3e7, v8
	v_mad_u32_u24 v8, v8, s9, v5
	v_lshlrev_b32_e32 v8, 2, v8
	global_load_dword v16, v8, s[4:5]
	v_add_u32_e32 v8, 4, v7
	v_min_u32_e32 v8, 0x3e7, v8
	v_mad_u32_u24 v8, v8, s9, v5
	v_lshlrev_b32_e32 v8, 2, v8
	global_load_dword v17, v8, s[4:5]
	v_add_u32_e32 v8, 8, v7
	v_min_u32_e32 v8, 0x3e7, v8
	v_mad_u32_u24 v8, v8, s9, v5
	v_lshlrev_b32_e32 v8, 2, v8
	global_load_dword v18, v8, s[4:5]
	v_add_u32_e32 v8, 12, v7
	v_min_u32_e32 v8, 0x3e7, v8
	v_mad_u32_u24 v8, v8, s9, v5
	v_lshlrev_b32_e32 v8, 2, v8
	global_load_dword v19, v8, s[4:5]
	v_add_u32_e32 v8, 16, v7
	v_min_u32_e32 v8, 0x3e7, v8
	v_mad_u32_u24 v8, v8, s9, v5
	v_lshlrev_b32_e32 v8, 2, v8
	global_load_dword v20, v8, s[4:5]
	v_add_u32_e32 v8, 20, v7
	v_min_u32_e32 v8, 0x3e7, v8
	v_mad_u32_u24 v8, v8, s9, v5
	v_lshlrev_b32_e32 v8, 2, v8
	global_load_dword v21, v8, s[4:5]
	v_add_u32_e32 v8, 24, v7
	v_min_u32_e32 v8, 0x3e7, v8
	v_mad_u32_u24 v8, v8, s9, v5
	v_lshlrev_b32_e32 v8, 2, v8
	global_load_dword v22, v8, s[4:5]
	v_add_u32_e32 v8, 28, v7
	v_min_u32_e32 v8, 0x3e7, v8
	v_mad_u32_u24 v8, v8, s9, v5
	v_lshlrev_b32_e32 v8, 2, v8
	global_load_dword v23, v8, s[4:5]
	v_add_u32_e32 v8, 32, v7
	v_min_u32_e32 v8, 0x3e7, v8
	v_mad_u32_u24 v8, v8, s9, v5
	v_lshlrev_b32_e32 v8, 2, v8
	global_load_dword v24, v8, s[4:5]
	v_add_u32_e32 v8, 36, v7
	v_min_u32_e32 v8, 0x3e7, v8
	v_mad_u32_u24 v8, v8, s9, v5
	v_lshlrev_b32_e32 v8, 2, v8
	global_load_dword v25, v8, s[4:5]
	v_add_u32_e32 v8, 40, v7
	v_min_u32_e32 v8, 0x3e7, v8
	v_mad_u32_u24 v8, v8, s9, v5
	v_lshlrev_b32_e32 v8, 2, v8
	global_load_dword v26, v8, s[4:5]
	v_add_u32_e32 v8, 44, v7
	v_min_u32_e32 v8, 0x3e7, v8
	v_mad_u32_u24 v8, v8, s9, v5
	v_lshlrev_b32_e32 v8, 2, v8
	global_load_dword v27, v8, s[4:5]
	v_add_u32_e32 v8, 48, v7
	v_min_u32_e32 v8, 0x3e7, v8
	v_mad_u32_u24 v8, v8, s9, v5
	v_lshlrev_b32_e32 v8, 2, v8
	global_load_dword v28, v8, s[4:5]
	v_add_u32_e32 v8, 52, v7
	v_min_u32_e32 v8, 0x3e7, v8
	v_mad_u32_u24 v8, v8, s9, v5
	v_lshlrev_b32_e32 v8, 2, v8
	global_load_dword v29, v8, s[4:5]
	v_add_u32_e32 v8, 56, v7
	v_min_u32_e32 v8, 0x3e7, v8
	v_mad_u32_u24 v8, v8, s9, v5
	v_lshlrev_b32_e32 v8, 2, v8
	global_load_dword v30, v8, s[4:5]
	v_add_u32_e32 v8, 60, v7
	v_min_u32_e32 v8, 0x3e7, v8
	v_mad_u32_u24 v8, v8, s9, v5
	v_lshlrev_b32_e32 v8, 2, v8
	global_load_dword v31, v8, s[4:5]
	v_cmp_gt_u32_e32 vcc, 0x3e8, v7
	s_and_b64 vcc, vcc, s[10:11]
	s_waitcnt vmcnt(15)
	v_cndmask_b32_e32 v16, 0, v16, vcc
	ds_write_b32 v9, v16
	v_cmp_gt_u32_e32 vcc, 0x3e4, v7
	s_and_b64 vcc, vcc, s[10:11]
	s_waitcnt vmcnt(14)
	v_cndmask_b32_e32 v17, 0, v17, vcc
	ds_write_b32 v9, v17 offset:1040
	v_cmp_gt_u32_e32 vcc, 0x3e0, v7
	s_and_b64 vcc, vcc, s[10:11]
	s_waitcnt vmcnt(13)
	v_cndmask_b32_e32 v18, 0, v18, vcc
	ds_write_b32 v9, v18 offset:2080
	v_cmp_gt_u32_e32 vcc, 0x3dc, v7
	s_and_b64 vcc, vcc, s[10:11]
	s_waitcnt vmcnt(12)
	v_cndmask_b32_e32 v19, 0, v19, vcc
	ds_write_b32 v9, v19 offset:3120
	v_cmp_gt_u32_e32 vcc, 0x3d8, v7
	s_and_b64 vcc, vcc, s[10:11]
	s_waitcnt vmcnt(11)
	v_cndmask_b32_e32 v20, 0, v20, vcc
	ds_write_b32 v9, v20 offset:4160
	v_cmp_gt_u32_e32 vcc, 0x3d4, v7
	s_and_b64 vcc, vcc, s[10:11]
	s_waitcnt vmcnt(10)
	v_cndmask_b32_e32 v21, 0, v21, vcc
	ds_write_b32 v9, v21 offset:5200
	v_cmp_gt_u32_e32 vcc, 0x3d0, v7
	s_and_b64 vcc, vcc, s[10:11]
	s_waitcnt vmcnt(9)
	v_cndmask_b32_e32 v22, 0, v22, vcc
	ds_write_b32 v9, v22 offset:6240
	v_cmp_gt_u32_e32 vcc, 0x3cc, v7
	s_and_b64 vcc, vcc, s[10:11]
	s_waitcnt vmcnt(8)
	v_cndmask_b32_e32 v23, 0, v23, vcc
	ds_write_b32 v9, v23 offset:7280
	v_cmp_gt_u32_e32 vcc, 0x3c8, v7
	s_and_b64 vcc, vcc, s[10:11]
	s_waitcnt vmcnt(7)
	v_cndmask_b32_e32 v24, 0, v24, vcc
	ds_write_b32 v9, v24 offset:8320
	v_cmp_gt_u32_e32 vcc, 0x3c4, v7
	s_and_b64 vcc, vcc, s[10:11]
	s_waitcnt vmcnt(6)
	v_cndmask_b32_e32 v25, 0, v25, vcc
	ds_write_b32 v9, v25 offset:9360
	v_cmp_gt_u32_e32 vcc, 0x3c0, v7
	s_and_b64 vcc, vcc, s[10:11]
	s_waitcnt vmcnt(5)
	v_cndmask_b32_e32 v26, 0, v26, vcc
	ds_write_b32 v9, v26 offset:10400
	v_cmp_gt_u32_e32 vcc, 0x3bc, v7
	s_and_b64 vcc, vcc, s[10:11]
	s_waitcnt vmcnt(4)
	v_cndmask_b32_e32 v27, 0, v27, vcc
	ds_write_b32 v9, v27 offset:11440
	v_cmp_gt_u32_e32 vcc, 0x3b8, v7
	s_and_b64 vcc, vcc, s[10:11]
	s_waitcnt vmcnt(3)
	v_cndmask_b32_e32 v28, 0, v28, vcc
	ds_write_b32 v9, v28 offset:12480
	v_cmp_gt_u32_e32 vcc, 0x3b4, v7
	s_and_b64 vcc, vcc, s[10:11]
	s_waitcnt vmcnt(2)
	v_cndmask_b32_e32 v29, 0, v29, vcc
	ds_write_b32 v9, v29 offset:13520
	v_cmp_gt_u32_e32 vcc, 0x3b0, v7
	s_and_b64 vcc, vcc, s[10:11]
	s_waitcnt vmcnt(1)
	v_cndmask_b32_e32 v30, 0, v30, vcc
	ds_write_b32 v9, v30 offset:14560
	v_cmp_gt_u32_e32 vcc, 0x3ac, v7
	s_and_b64 vcc, vcc, s[10:11]
	s_waitcnt vmcnt(0)
	v_cndmask_b32_e32 v31, 0, v31, vcc
	ds_write_b32 v9, v31 offset:15600
	v_lshrrev_b32_e32 v1, 2, v0
	v_and_b32_e32 v12, 3, v0
	v_and_b32_e32 v2, 0xfc, v0
	s_movk_i32 s4, 0x820
	v_add_u32_e32 v6, s8, v1
	v_mad_u32_u24 v1, v12, s4, v2
	s_waitcnt lgkmcnt(0)
	s_barrier
	ds_read2_b32 v[2:3], v1 offset1:65
	ds_read2_b32 v[10:11], v1 offset0:130 offset1:195
	v_mov_b32_e32 v7, 0
	v_lshlrev_b64 v[4:5], 11, v[6:7]
	s_mov_b32 s4, 0x45000000
	v_lshl_add_u64 v[8:9], s[6:7], 0, v[4:5]
	s_waitcnt lgkmcnt(1)
	v_fma_mixlo_f16 v4, v2, s4, 0
	v_mov_b32_e32 v2, v3
	s_waitcnt lgkmcnt(0)
	v_mov_b32_e32 v3, v10
	v_add_u32_e32 v6, 0x400, v1
	ds_read2_b32 v[14:15], v6 offset0:4 offset1:69
	v_pk_mul_f32 v[2:3], v[2:3], s[4:5] op_sel_hi:[1,0]
	s_waitcnt lgkmcnt(0)
	v_mov_b32_e32 v5, v14
	v_cvt_pk_f16_f32 v3, v2, v3
	v_pack_b32_f16 v2, v4, v3
	v_mov_b32_e32 v4, v11
	ds_read2_b32 v[10:11], v6 offset0:134 offset1:199
	v_pk_mul_f32 v[4:5], v[4:5], s[4:5] op_sel_hi:[1,0]
	s_nop 0
	v_cvt_pk_f16_f32 v6, v4, v5
	v_mov_b32_e32 v4, v15
	s_waitcnt lgkmcnt(0)
	v_mov_b32_e32 v5, v10
	v_pk_mul_f32 v[4:5], v[4:5], s[4:5] op_sel_hi:[1,0]
	v_alignbit_b32 v3, v6, v3, 16
	v_cvt_pk_f16_f32 v5, v4, v5
	v_alignbit_b32 v4, v5, v6, 16
	v_lshlrev_b32_e32 v6, 4, v12
	v_lshrrev_b32_e32 v5, 16, v5
	v_lshl_or_b32 v6, s3, 1, v6
	v_fma_mixhi_f16 v5, v11, s4, 0
	v_lshl_add_u64 v[10:11], v[8:9], 0, v[6:7]
	global_store_dwordx4 v[10:11], v[2:5], off
	v_or_b32_e32 v6, 64, v6
	v_lshl_add_u64 v[6:7], v[8:9], 0, v[6:7]
	v_add_u32_e32 v4, 0x2000, v1
	ds_read2_b32 v[2:3], v4 offset0:32 offset1:97
	ds_read2_b32 v[4:5], v4 offset0:162 offset1:227
	v_add_u32_e32 v1, 0x2400, v1
	ds_read2_b32 v[12:13], v1 offset0:36 offset1:101
	ds_read2_b32 v[10:11], v1 offset0:166 offset1:231
	s_waitcnt lgkmcnt(3)
	v_fma_mixlo_f16 v1, v2, s4, 0
	v_mov_b32_e32 v2, v3
	s_waitcnt lgkmcnt(2)
	v_mov_b32_e32 v3, v4
	v_pk_mul_f32 v[2:3], v[2:3], s[4:5] op_sel_hi:[1,0]
	v_mov_b32_e32 v4, v5
	s_waitcnt lgkmcnt(1)
	v_mov_b32_e32 v5, v12
	v_cvt_pk_f16_f32 v3, v2, v3
	v_pk_mul_f32 v[4:5], v[4:5], s[4:5] op_sel_hi:[1,0]
	v_pack_b32_f16 v2, v1, v3
	v_cvt_pk_f16_f32 v1, v4, v5
	v_mov_b32_e32 v4, v13
	s_waitcnt lgkmcnt(0)
	v_mov_b32_e32 v5, v10
	v_pk_mul_f32 v[4:5], v[4:5], s[4:5] op_sel_hi:[1,0]
	v_alignbit_b32 v3, v1, v3, 16
	v_cvt_pk_f16_f32 v5, v4, v5
	v_alignbit_b32 v4, v5, v1, 16
	v_lshrrev_b32_e32 v5, 16, v5
	v_fma_mixhi_f16 v5, v11, s4, 0
	global_store_dwordx4 v[6:7], v[2:5], off

.LBB0_81:
	s_load_dwordx2 s[6:7], s[0:1], 0x10
	s_lshl_b32 s5, s2, 1
	s_andn2_b32 s5, s5, 63
	s_lshl_b32 s4, s2, 6
	s_and_b32 s4, s4, 0x7c0
	s_load_dwordx2 s[2:3], s[0:1], 0x28
	v_and_b32_e32 v6, 63, v0
	v_lshrrev_b32_e32 v1, 6, v0
	v_or_b32_e32 v4, s5, v6
	s_movk_i32 s9, 0x3e8
	v_cmp_gt_u32_e32 vcc, 0x3e8, v4
	v_min_u32_e32 v5, 0x3e7, v4
	v_add_u32_e32 v7, s4, v1
	s_mov_b64 s[10:11], vcc
	v_mul_u32_u24_e32 v9, 0x104, v1
	v_lshl_add_u32 v9, v6, 2, v9
	s_waitcnt lgkmcnt(0)
	v_add_u32_e32 v8, 0, v7
	v_min_u32_e32 v8, 0x7ff, v8
	v_mad_u32_u24 v8, v8, s9, v5
	v_lshlrev_b32_e32 v8, 2, v8
	global_load_dword v16, v8, s[6:7]
	v_add_u32_e32 v8, 4, v7
	v_min_u32_e32 v8, 0x7ff, v8
	v_mad_u32_u24 v8, v8, s9, v5
	v_lshlrev_b32_e32 v8, 2, v8
	global_load_dword v17, v8, s[6:7]
	v_add_u32_e32 v8, 8, v7
	v_min_u32_e32 v8, 0x7ff, v8
	v_mad_u32_u24 v8, v8, s9, v5
	v_lshlrev_b32_e32 v8, 2, v8
	global_load_dword v18, v8, s[6:7]
	v_add_u32_e32 v8, 12, v7
	v_min_u32_e32 v8, 0x7ff, v8
	v_mad_u32_u24 v8, v8, s9, v5
	v_lshlrev_b32_e32 v8, 2, v8
	global_load_dword v19, v8, s[6:7]
	v_add_u32_e32 v8, 16, v7
	v_min_u32_e32 v8, 0x7ff, v8
	v_mad_u32_u24 v8, v8, s9, v5
	v_lshlrev_b32_e32 v8, 2, v8
	global_load_dword v20, v8, s[6:7]
	v_add_u32_e32 v8, 20, v7
	v_min_u32_e32 v8, 0x7ff, v8
	v_mad_u32_u24 v8, v8, s9, v5
	v_lshlrev_b32_e32 v8, 2, v8
	global_load_dword v21, v8, s[6:7]
	v_add_u32_e32 v8, 24, v7
	v_min_u32_e32 v8, 0x7ff, v8
	v_mad_u32_u24 v8, v8, s9, v5
	v_lshlrev_b32_e32 v8, 2, v8
	global_load_dword v22, v8, s[6:7]
	v_add_u32_e32 v8, 28, v7
	v_min_u32_e32 v8, 0x7ff, v8
	v_mad_u32_u24 v8, v8, s9, v5
	v_lshlrev_b32_e32 v8, 2, v8
	global_load_dword v23, v8, s[6:7]
	v_add_u32_e32 v8, 32, v7
	v_min_u32_e32 v8, 0x7ff, v8
	v_mad_u32_u24 v8, v8, s9, v5
	v_lshlrev_b32_e32 v8, 2, v8
	global_load_dword v24, v8, s[6:7]
	v_add_u32_e32 v8, 36, v7
	v_min_u32_e32 v8, 0x7ff, v8
	v_mad_u32_u24 v8, v8, s9, v5
	v_lshlrev_b32_e32 v8, 2, v8
	global_load_dword v25, v8, s[6:7]
	v_add_u32_e32 v8, 40, v7
	v_min_u32_e32 v8, 0x7ff, v8
	v_mad_u32_u24 v8, v8, s9, v5
	v_lshlrev_b32_e32 v8, 2, v8
	global_load_dword v26, v8, s[6:7]
	v_add_u32_e32 v8, 44, v7
	v_min_u32_e32 v8, 0x7ff, v8
	v_mad_u32_u24 v8, v8, s9, v5
	v_lshlrev_b32_e32 v8, 2, v8
	global_load_dword v27, v8, s[6:7]
	v_add_u32_e32 v8, 48, v7
	v_min_u32_e32 v8, 0x7ff, v8
	v_mad_u32_u24 v8, v8, s9, v5
	v_lshlrev_b32_e32 v8, 2, v8
	global_load_dword v28, v8, s[6:7]
	v_add_u32_e32 v8, 52, v7
	v_min_u32_e32 v8, 0x7ff, v8
	v_mad_u32_u24 v8, v8, s9, v5
	v_lshlrev_b32_e32 v8, 2, v8
	global_load_dword v29, v8, s[6:7]
	v_add_u32_e32 v8, 56, v7
	v_min_u32_e32 v8, 0x7ff, v8
	v_mad_u32_u24 v8, v8, s9, v5
	v_lshlrev_b32_e32 v8, 2, v8
	global_load_dword v30, v8, s[6:7]
	v_add_u32_e32 v8, 60, v7
	v_min_u32_e32 v8, 0x7ff, v8
	v_mad_u32_u24 v8, v8, s9, v5
	v_lshlrev_b32_e32 v8, 2, v8
	global_load_dword v31, v8, s[6:7]
	v_cmp_gt_u32_e32 vcc, 0x800, v7
	s_and_b64 vcc, vcc, s[10:11]
	s_waitcnt vmcnt(15)
	v_cndmask_b32_e32 v16, 0, v16, vcc
	ds_write_b32 v9, v16
	v_cmp_gt_u32_e32 vcc, 0x7fc, v7
	s_and_b64 vcc, vcc, s[10:11]
	s_waitcnt vmcnt(14)
	v_cndmask_b32_e32 v17, 0, v17, vcc
	ds_write_b32 v9, v17 offset:1040
	v_cmp_gt_u32_e32 vcc, 0x7f8, v7
	s_and_b64 vcc, vcc, s[10:11]
	s_waitcnt vmcnt(13)
	v_cndmask_b32_e32 v18, 0, v18, vcc
	ds_write_b32 v9, v18 offset:2080
	v_cmp_gt_u32_e32 vcc, 0x7f4, v7
	s_and_b64 vcc, vcc, s[10:11]
	s_waitcnt vmcnt(12)
	v_cndmask_b32_e32 v19, 0, v19, vcc
	ds_write_b32 v9, v19 offset:3120
	v_cmp_gt_u32_e32 vcc, 0x7f0, v7
	s_and_b64 vcc, vcc, s[10:11]
	s_waitcnt vmcnt(11)
	v_cndmask_b32_e32 v20, 0, v20, vcc
	ds_write_b32 v9, v20 offset:4160
	v_cmp_gt_u32_e32 vcc, 0x7ec, v7
	s_and_b64 vcc, vcc, s[10:11]
	s_waitcnt vmcnt(10)
	v_cndmask_b32_e32 v21, 0, v21, vcc
	ds_write_b32 v9, v21 offset:5200
	v_cmp_gt_u32_e32 vcc, 0x7e8, v7
	s_and_b64 vcc, vcc, s[10:11]
	s_waitcnt vmcnt(9)
	v_cndmask_b32_e32 v22, 0, v22, vcc
	ds_write_b32 v9, v22 offset:6240
	v_cmp_gt_u32_e32 vcc, 0x7e4, v7
	s_and_b64 vcc, vcc, s[10:11]
	s_waitcnt vmcnt(8)
	v_cndmask_b32_e32 v23, 0, v23, vcc
	ds_write_b32 v9, v23 offset:7280
	v_cmp_gt_u32_e32 vcc, 0x7e0, v7
	s_and_b64 vcc, vcc, s[10:11]
	s_waitcnt vmcnt(7)
	v_cndmask_b32_e32 v24, 0, v24, vcc
	ds_write_b32 v9, v24 offset:8320
	v_cmp_gt_u32_e32 vcc, 0x7dc, v7
	s_and_b64 vcc, vcc, s[10:11]
	s_waitcnt vmcnt(6)
	v_cndmask_b32_e32 v25, 0, v25, vcc
	ds_write_b32 v9, v25 offset:9360
	v_cmp_gt_u32_e32 vcc, 0x7d8, v7
	s_and_b64 vcc, vcc, s[10:11]
	s_waitcnt vmcnt(5)
	v_cndmask_b32_e32 v26, 0, v26, vcc
	ds_write_b32 v9, v26 offset:10400
	v_cmp_gt_u32_e32 vcc, 0x7d4, v7
	s_and_b64 vcc, vcc, s[10:11]
	s_waitcnt vmcnt(4)
	v_cndmask_b32_e32 v27, 0, v27, vcc
	ds_write_b32 v9, v27 offset:11440
	v_cmp_gt_u32_e32 vcc, 0x7d0, v7
	s_and_b64 vcc, vcc, s[10:11]
	s_waitcnt vmcnt(3)
	v_cndmask_b32_e32 v28, 0, v28, vcc
	ds_write_b32 v9, v28 offset:12480
	v_cmp_gt_u32_e32 vcc, 0x7cc, v7
	s_and_b64 vcc, vcc, s[10:11]
	s_waitcnt vmcnt(2)
	v_cndmask_b32_e32 v29, 0, v29, vcc
	ds_write_b32 v9, v29 offset:13520
	v_cmp_gt_u32_e32 vcc, 0x7c8, v7
	s_and_b64 vcc, vcc, s[10:11]
	s_waitcnt vmcnt(1)
	v_cndmask_b32_e32 v30, 0, v30, vcc
	ds_write_b32 v9, v30 offset:14560
	v_cmp_gt_u32_e32 vcc, 0x7c4, v7
	s_and_b64 vcc, vcc, s[10:11]
	s_waitcnt vmcnt(0)
	v_cndmask_b32_e32 v31, 0, v31, vcc
	ds_write_b32 v9, v31 offset:15600
	v_lshrrev_b32_e32 v1, 2, v0
	v_and_b32_e32 v12, 3, v0
	v_and_b32_e32 v0, 0xfc, v0
	v_add_u32_e32 v1, s5, v1
	s_movk_i32 s0, 0x820
	v_ashrrev_i32_e32 v4, 7, v1
	v_lshlrev_b32_e32 v1, 7, v1
	v_mad_u32_u24 v13, v12, s0, v0
	s_waitcnt lgkmcnt(0)
	s_barrier
	v_and_b32_e32 v6, 0x3f80, v1
	ds_read2_b32 v[0:1], v13 offset1:65
	ds_read2_b32 v[10:11], v13 offset0:130 offset1:195
	v_mov_b32_e32 v7, 0
	v_lshl_add_u64 v[8:9], s[2:3], 0, v[6:7]
	s_mov_b32 s2, 0x45000000
	s_waitcnt lgkmcnt(1)
	v_fma_mixlo_f16 v2, v0, s2, 0
	v_mov_b32_e32 v0, v1
	s_waitcnt lgkmcnt(0)
	v_mov_b32_e32 v1, v10
	v_add_u32_e32 v6, 0x400, v13
	ds_read2_b32 v[14:15], v6 offset0:4 offset1:69
	v_pk_mul_f32 v[0:1], v[0:1], s[2:3] op_sel_hi:[1,0]
	v_ashrrev_i32_e32 v5, 31, v4
	v_cvt_pk_f16_f32 v1, v0, v1
	v_pack_b32_f16 v0, v2, v1
	v_mov_b32_e32 v2, v11
	ds_read2_b32 v[10:11], v6 offset0:134 offset1:199
	s_waitcnt lgkmcnt(1)
	v_mov_b32_e32 v3, v14
	v_pk_mul_f32 v[2:3], v[2:3], s[2:3] op_sel_hi:[1,0]
	v_lshlrev_b64 v[4:5], 19, v[4:5]
	v_cvt_pk_f16_f32 v6, v2, v3
	v_mov_b32_e32 v2, v15
	s_waitcnt lgkmcnt(0)
	v_mov_b32_e32 v3, v10
	v_pk_mul_f32 v[2:3], v[2:3], s[2:3] op_sel_hi:[1,0]
	s_mov_b32 s1, 0
	v_cvt_pk_f16_f32 v3, v2, v3
	s_lshl_b32 s0, s4, 8
	v_lshl_add_u64 v[4:5], v[8:9], 0, v[4:5]
	v_alignbit_b32 v1, v6, v1, 16
	v_alignbit_b32 v2, v3, v6, 16
	v_lshrrev_b32_e32 v3, 16, v3
	v_lshl_add_u64 v[4:5], v[4:5], 0, s[0:1]
	v_lshlrev_b32_e32 v6, 4, v12
	v_fma_mixhi_f16 v3, v11, s2, 0
	v_lshl_add_u64 v[8:9], v[4:5], 0, v[6:7]
	global_store_dwordx4 v[8:9], v[0:3], off
	v_or_b32_e32 v6, 64, v6
	v_lshl_add_u64 v[4:5], v[4:5], 0, v[6:7]
	v_add_u32_e32 v2, 0x2000, v13
	ds_read2_b32 v[0:1], v2 offset0:32 offset1:97
	ds_read2_b32 v[10:11], v2 offset0:162 offset1:227
	v_add_u32_e32 v2, 0x2400, v13
	ds_read2_b32 v[12:13], v2 offset0:36 offset1:101
	ds_read2_b32 v[8:9], v2 offset0:166 offset1:231
	s_waitcnt lgkmcnt(3)
	v_fma_mixlo_f16 v2, v0, s2, 0
	v_mov_b32_e32 v0, v1
	s_waitcnt lgkmcnt(2)
	v_mov_b32_e32 v1, v10
	v_pk_mul_f32 v[0:1], v[0:1], s[2:3] op_sel_hi:[1,0]
	s_waitcnt lgkmcnt(1)
	v_mov_b32_e32 v3, v12
	v_cvt_pk_f16_f32 v1, v0, v1
	v_pack_b32_f16 v0, v2, v1
	v_mov_b32_e32 v2, v11
	v_pk_mul_f32 v[2:3], v[2:3], s[2:3] op_sel_hi:[1,0]
	s_nop 0
	v_cvt_pk_f16_f32 v6, v2, v3
	v_mov_b32_e32 v2, v13
	s_waitcnt lgkmcnt(0)
	v_mov_b32_e32 v3, v8
	v_pk_mul_f32 v[2:3], v[2:3], s[2:3] op_sel_hi:[1,0]
	v_alignbit_b32 v1, v6, v1, 16
	v_cvt_pk_f16_f32 v3, v2, v3
	v_alignbit_b32 v2, v3, v6, 16
	v_lshrrev_b32_e32 v3, 16, v3
	v_fma_mixhi_f16 v3, v9, s2, 0
	global_store_dwordx4 v[4:5], v[0:3], off
	s_endpgm

	.amdhsa_kernel _Z8prep_allPKfPcS0_S0_S0_S1_S1_S1_PyPiS3_
		.amdhsa_group_segment_fixed_size 16640
		.amdhsa_private_segment_fixed_size 0
		.amdhsa_kernarg_size 88
		.amdhsa_user_sgpr_count 2
		.amdhsa_user_sgpr_dispatch_ptr 0
		.amdhsa_user_sgpr_queue_ptr 0
		.amdhsa_user_sgpr_kernarg_segment_ptr 1
		.amdhsa_user_sgpr_dispatch_id 0
		.amdhsa_user_sgpr_kernarg_preload_length 0
		.amdhsa_user_sgpr_kernarg_preload_offset 0
		.amdhsa_user_sgpr_private_segment_size 0
		.amdhsa_uses_dynamic_stack 0
		.amdhsa_enable_private_segment 0
		.amdhsa_system_sgpr_workgroup_id_x 1
		.amdhsa_system_sgpr_workgroup_id_y 0
		.amdhsa_system_sgpr_workgroup_id_z 0
		.amdhsa_system_sgpr_workgroup_info 0
		.amdhsa_system_vgpr_workitem_id 0
		.amdhsa_next_free_vgpr 48
		.amdhsa_next_free_sgpr 24
		.amdhsa_accum_offset 48
		.amdhsa_reserve_vcc 1
		.amdhsa_float_round_mode_32 0
		.amdhsa_float_round_mode_16_64 0
		.amdhsa_float_denorm_mode_32 3
		.amdhsa_float_denorm_mode_16_64 3
		.amdhsa_dx10_clamp 1
		.amdhsa_ieee_mode 1
		.amdhsa_fp16_overflow 0
		.amdhsa_tg_split 0
		.amdhsa_exception_fp_ieee_invalid_op 0
		.amdhsa_exception_fp_denorm_src 0
		.amdhsa_exception_fp_ieee_div_zero 0
		.amdhsa_exception_fp_ieee_overflow 0
		.amdhsa_exception_fp_ieee_underflow 0
		.amdhsa_exception_fp_ieee_inexact 0
		.amdhsa_exception_int_div_zero 0
	.end_amdhsa_kernel

_Z12final_kernelPKfPKiPK15HIP_vector_typeIiLj4EES2_S2_S0_S0_S0_S0_Pf:
	s_load_dwordx2 s[4:5], s[0:1], 0x10
	s_ashr_i32 s3, s2, 31
	s_lshl_b64 s[6:7], s[2:3], 4
	s_waitcnt lgkmcnt(0)
	s_add_u32 s4, s4, s6
	s_addc_u32 s5, s5, s7
	s_load_dwordx4 s[4:7], s[4:5], 0x0
	s_waitcnt lgkmcnt(0)
	s_cmp_eq_u32 s6, 0
	s_cbranch_scc1 .LBB4_17
	s_load_dwordx2 s[12:13], s[0:1], 0x8
	s_load_dwordx2 s[18:19], s[0:1], 0x0
	s_load_dwordx4 s[8:11], s[0:1], 0x20
	s_load_dwordx2 s[16:17], s[0:1], 0x30
	s_movk_i32 s20, 0x51f
	s_add_i32 s21, s6, -1
	v_add_u32_e32 v1, 0x100, v0
	v_add_u32_e32 v2, 0x200, v0
	v_add_u32_e32 v3, 0x300, v0
	v_min_u32_e32 v3, 0x31f, v3
	v_mul_u32_u24_e32 v4, s20, v0
	v_mul_u32_u24_e32 v5, s20, v1
	v_mul_u32_u24_e32 v6, s20, v2
	v_mul_u32_u24_e32 v7, s20, v3
	v_lshrrev_b32_e32 v4, 15, v4
	v_lshrrev_b32_e32 v5, 15, v5
	v_lshrrev_b32_e32 v6, 15, v6
	v_lshrrev_b32_e32 v7, 15, v7
	v_mul_u32_u24_e32 v8, 25, v4
	v_mul_u32_u24_e32 v9, 25, v5
	v_mul_u32_u24_e32 v10, 25, v6
	v_mul_u32_u24_e32 v11, 25, v7
	v_sub_u32_e32 v8, v0, v8
	v_sub_u32_e32 v9, v1, v9
	v_sub_u32_e32 v10, v2, v10
	v_sub_u32_e32 v11, v3, v11
	v_min_u32_e32 v12, s21, v4
	v_min_u32_e32 v13, s21, v5
	v_min_u32_e32 v14, s21, v6
	v_min_u32_e32 v15, s21, v7
	v_add_lshl_u32 v12, v12, s5, 2
	v_add_lshl_u32 v13, v13, s5, 2
	v_add_lshl_u32 v14, v14, s5, 2
	v_add_lshl_u32 v15, v15, s5, 2
	s_waitcnt lgkmcnt(0)
	global_load_dword v12, v12, s[12:13]
	global_load_dword v13, v13, s[12:13]
	global_load_dword v14, v14, s[12:13]
	global_load_dword v15, v15, s[12:13]
	s_mul_i32 s22, s2, 0xc800
	s_add_u32 s24, s18, s22
	s_addc_u32 s25, s19, 0
	s_add_u32 s26, s24, 0x3200
	s_addc_u32 s27, s25, 0
	s_add_u32 s28, s24, 0x6400
	s_addc_u32 s29, s25, 0
	s_add_u32 s30, s24, 0x9600
	s_addc_u32 s31, s25, 0
	s_mul_i32 s22, s4, 0x190
	s_add_u32 s16, s16, s22
	s_addc_u32 s17, s17, 0
	s_mul_i32 s32, s4, 0x864
	s_addk_i32 s32, 0x800
	s_movk_i32 s33, 0x190
	v_lshlrev_b32_e32 v112, 4, v0
	v_lshlrev_b32_e32 v113, 4, v1
	v_lshlrev_b32_e32 v114, 4, v2
	v_lshlrev_b32_e32 v115, 4, v3
	v_lshlrev_b32_e32 v116, 4, v8
	v_lshlrev_b32_e32 v117, 4, v9
	v_lshlrev_b32_e32 v118, 4, v10
	v_lshlrev_b32_e32 v119, 4, v11
	s_waitcnt vmcnt(0)
	v_lshlrev_b32_e32 v12, 2, v12
	v_lshlrev_b32_e32 v13, 2, v13
	v_lshlrev_b32_e32 v14, 2, v14
	v_lshlrev_b32_e32 v15, 2, v15
	global_load_dword v12, v12, s[8:9]
	global_load_dword v13, v13, s[8:9]
	global_load_dword v14, v14, s[8:9]
	global_load_dword v15, v15, s[8:9]
	s_waitcnt vmcnt(0)
	v_add_u32_e32 v12, s32, v12
	v_add_u32_e32 v13, s32, v13
	v_add_u32_e32 v14, s32, v14
	v_add_u32_e32 v15, s32, v15
	v_mad_u32_u24 v120, v12, s33, v116
	v_mad_u32_u24 v121, v13, s33, v117
	v_mad_u32_u24 v122, v14, s33, v118
	v_mad_u32_u24 v123, v15, s33, v119
	global_load_dwordx4 v[16:19], v120, s[10:11]
	global_load_dwordx4 v[20:23], v116, s[16:17]
	global_load_dwordx4 v[24:27], v112, s[24:25]
	global_load_dwordx4 v[28:31], v112, s[26:27]
	global_load_dwordx4 v[32:35], v112, s[28:29]
	global_load_dwordx4 v[36:39], v112, s[30:31]
	global_load_dwordx4 v[40:43], v121, s[10:11]
	global_load_dwordx4 v[44:47], v117, s[16:17]
	global_load_dwordx4 v[48:51], v113, s[24:25]
	global_load_dwordx4 v[52:55], v113, s[26:27]
	global_load_dwordx4 v[56:59], v113, s[28:29]
	global_load_dwordx4 v[60:63], v113, s[30:31]
	global_load_dwordx4 v[64:67], v122, s[10:11]
	global_load_dwordx4 v[68:71], v118, s[16:17]
	global_load_dwordx4 v[72:75], v114, s[24:25]
	global_load_dwordx4 v[76:79], v114, s[26:27]
	global_load_dwordx4 v[80:83], v114, s[28:29]
	global_load_dwordx4 v[84:87], v114, s[30:31]
	global_load_dwordx4 v[88:91], v123, s[10:11]
	global_load_dwordx4 v[92:95], v119, s[16:17]
	global_load_dwordx4 v[96:99], v115, s[24:25]
	global_load_dwordx4 v[100:103], v115, s[26:27]
	global_load_dwordx4 v[104:107], v115, s[28:29]
	global_load_dwordx4 v[108:111], v115, s[30:31]
	s_waitcnt vmcnt(18)
	v_pk_add_f32 v[24:25], v[24:25], v[28:29]
	v_pk_add_f32 v[26:27], v[26:27], v[30:31]
	v_pk_add_f32 v[32:33], v[32:33], v[36:37]
	v_pk_add_f32 v[34:35], v[34:35], v[38:39]
	v_pk_add_f32 v[24:25], v[24:25], v[32:33]
	v_pk_add_f32 v[26:27], v[26:27], v[34:35]
	v_pk_add_f32 v[16:17], v[20:21], v[16:17]
	v_pk_add_f32 v[18:19], v[22:23], v[18:19]
	v_pk_add_f32 v[24:25], v[24:25], v[16:17]
	v_pk_add_f32 v[26:27], v[26:27], v[18:19]
	v_max_f32_e32 v24, 0, v24
	v_max_f32_e32 v25, 0, v25
	v_max_f32_e32 v26, 0, v26
	v_max_f32_e32 v27, 0, v27
	ds_write_b128 v112, v[24:27]
	s_waitcnt vmcnt(12)
	v_pk_add_f32 v[48:49], v[48:49], v[52:53]
	v_pk_add_f32 v[50:51], v[50:51], v[54:55]
	v_pk_add_f32 v[56:57], v[56:57], v[60:61]
	v_pk_add_f32 v[58:59], v[58:59], v[62:63]
	v_pk_add_f32 v[48:49], v[48:49], v[56:57]
	v_pk_add_f32 v[50:51], v[50:51], v[58:59]
	v_pk_add_f32 v[40:41], v[44:45], v[40:41]
	v_pk_add_f32 v[42:43], v[46:47], v[42:43]
	v_pk_add_f32 v[48:49], v[48:49], v[40:41]
	v_pk_add_f32 v[50:51], v[50:51], v[42:43]
	v_max_f32_e32 v48, 0, v48
	v_max_f32_e32 v49, 0, v49
	v_max_f32_e32 v50, 0, v50
	v_max_f32_e32 v51, 0, v51
	ds_write_b128 v113, v[48:51]
	s_waitcnt vmcnt(6)
	v_pk_add_f32 v[72:73], v[72:73], v[76:77]
	v_pk_add_f32 v[74:75], v[74:75], v[78:79]
	v_pk_add_f32 v[80:81], v[80:81], v[84:85]
	v_pk_add_f32 v[82:83], v[82:83], v[86:87]
	v_pk_add_f32 v[72:73], v[72:73], v[80:81]
	v_pk_add_f32 v[74:75], v[74:75], v[82:83]
	v_pk_add_f32 v[64:65], v[68:69], v[64:65]
	v_pk_add_f32 v[66:67], v[70:71], v[66:67]
	v_pk_add_f32 v[72:73], v[72:73], v[64:65]
	v_pk_add_f32 v[74:75], v[74:75], v[66:67]
	v_max_f32_e32 v72, 0, v72
	v_max_f32_e32 v73, 0, v73
	v_max_f32_e32 v74, 0, v74
	v_max_f32_e32 v75, 0, v75
	ds_write_b128 v114, v[72:75]
	s_waitcnt vmcnt(0)
	v_pk_add_f32 v[96:97], v[96:97], v[100:101]
	v_pk_add_f32 v[98:99], v[98:99], v[102:103]
	v_pk_add_f32 v[104:105], v[104:105], v[108:109]
	v_pk_add_f32 v[106:107], v[106:107], v[110:111]
	v_pk_add_f32 v[96:97], v[96:97], v[104:105]
	v_pk_add_f32 v[98:99], v[98:99], v[106:107]
	v_pk_add_f32 v[88:89], v[92:93], v[88:89]
	v_pk_add_f32 v[90:91], v[94:95], v[90:91]
	v_pk_add_f32 v[96:97], v[96:97], v[88:89]
	v_pk_add_f32 v[98:99], v[98:99], v[90:91]
	v_max_f32_e32 v96, 0, v96
	v_max_f32_e32 v97, 0, v97
	v_max_f32_e32 v98, 0, v98
	v_max_f32_e32 v99, 0, v99
	ds_write_b128 v115, v[96:99]
	s_mov_b64 s[14:15], -1

.LBB4_17:
	s_endpgm
	.p2align 8

_Z7gemm_x3ILi2ELi2ELi2ELi0EEvPKcS1_iiPKfiS3_PKiPciPy:
	s_load_dwordx8 s[4:11], s[0:1], 0x0
	s_ashr_i32 s17, s2, 3
	s_abs_i32 s18, s17
	v_lshlrev_b32_e32 v170, 4, v0
	s_load_dword s16, s[0:1], 0x20
	s_load_dwordx4 s[12:15], s[0:1], 0x28
	s_waitcnt lgkmcnt(0)
	s_abs_i32 s3, s9
	v_cvt_f32_u32_e32 v2, s3
	s_sub_i32 s20, 0, s3
	s_xor_b32 s19, s17, s9
	s_ashr_i32 s19, s19, 31
	v_rcp_iflag_f32_e32 v2, v2
	v_bfe_u32 v19, v0, 6, 1
	v_and_b32_e32 v164, 31, v0
	v_mov_b32_e32 v155, 0
	v_mul_f32_e32 v2, 0x4f7ffffe, v2
	v_cvt_u32_f32_e32 v2, v2
	v_lshlrev_b32_e32 v165, 6, v19
	v_mov_b32_e32 v3, v155
	v_bfe_u32 v1, v0, 7, 1
	v_readfirstlane_b32 s21, v2
	s_mul_i32 s20, s20, s21
	s_mul_hi_u32 s20, s21, s20
	s_add_i32 s21, s21, s20
	s_mul_hi_u32 s20, s18, s21
	s_mul_i32 s21, s20, s3
	s_sub_i32 s18, s18, s21
	s_add_i32 s22, s20, 1
	s_sub_i32 s21, s18, s3
	s_cmp_ge_u32 s18, s3
	s_cselect_b32 s20, s22, s20
	s_cselect_b32 s18, s21, s18
	s_add_i32 s21, s20, 1
	s_cmp_ge_u32 s18, s3
	s_cselect_b32 s3, s21, s20
	s_xor_b32 s3, s3, s19
	s_sub_i32 s20, s3, s19
	s_mul_i32 s3, s20, s9
	s_sub_i32 s3, s17, s3
	s_lshl_b32 s2, s2, 7
	s_lshl_b32 s3, s3, 10
	s_and_b32 s2, s2, 0x380
	s_or_b32 s17, s3, s2
	s_ashr_i32 s9, s17, 7
	s_ashr_i32 s2, s8, 6
	s_ashr_i32 s18, s9, 31
	s_ashr_i32 s3, s2, 31
	s_lshl_b32 s21, s2, 14
	s_mul_i32 s18, s21, s18
	s_mul_hi_u32 s19, s21, s9
	s_lshr_b64 s[2:3], s[2:3], 18
	s_add_i32 s18, s19, s18
	s_mul_i32 s3, s2, s9
	s_add_i32 s3, s18, s3
	s_mul_i32 s9, s21, s9
	s_add_u32 s18, s6, s9
	s_addc_u32 s19, s7, s3
	s_movk_i32 s3, 0x70
	v_bitop3_b32 v154, v0, s3, v170 bitop3:0x48
	s_ashr_i32 s3, s20, 31
	s_mul_i32 s3, s21, s3
	s_mul_hi_u32 s6, s21, s20
	s_add_i32 s3, s6, s3
	s_mul_i32 s2, s2, s20
	s_add_i32 s6, s3, s2
	s_mul_i32 s7, s21, s20
	s_add_u32 s2, s4, s7
	s_addc_u32 s3, s5, s6
	v_and_b32_e32 v2, 0x1f80, v170
	v_or3_b32 v6, v165, s17, v164
	v_lshl_add_u64 v[4:5], s[2:3], 0, v[2:3]
	v_ashrrev_i32_e32 v7, 31, v6
	v_lshl_add_u64 v[146:147], v[4:5], 0, v[154:155]
	s_movk_i32 s9, 0x3f80
	v_mov_b32_e32 v4, 0x2000
	v_lshrrev_b32_e32 v168, 8, v0
	v_bfe_u32 v18, v0, 5, 1
	v_lshl_add_u64 v[6:7], v[6:7], 2, s[14:15]
	v_lshlrev_b32_e32 v166, 6, v1
	v_bitop3_b32 v4, v170, s9, v4 bitop3:0xc8
	global_load_dword v20, v[6:7], off
	global_load_dword v21, v[6:7], off offset:128
	s_lshl_b32 s9, s20, 7
	v_lshl_or_b32 v6, v168, 5, v166
	v_lshlrev_b32_e32 v167, 2, v18
	v_or3_b32 v14, v6, v167, s9
	v_cmp_gt_i32_e32 vcc, s16, v14
	v_or_b32_e32 v10, 8, v14
	v_mov_b32_e32 v5, v155
	v_cndmask_b32_e32 v6, 0, v14, vcc
	v_cmp_gt_i32_e32 vcc, s16, v10
	v_ashrrev_i32_e32 v7, 31, v6
	v_lshlrev_b64 v[6:7], 2, v[6:7]
	v_cndmask_b32_e32 v10, 0, v10, vcc
	v_ashrrev_i32_e32 v11, 31, v10
	v_lshl_add_u64 v[8:9], s[10:11], 0, v[6:7]
	v_lshlrev_b64 v[10:11], 2, v[10:11]
	v_lshl_add_u64 v[12:13], s[10:11], 0, v[10:11]
	global_load_dwordx4 v[78:81], v[8:9], off
	global_load_dwordx4 v[74:77], v[12:13], off
	v_or_b32_e32 v8, 16, v14
	v_cmp_gt_i32_e32 vcc, s16, v8
	v_or_b32_e32 v14, 24, v14
	v_lshl_add_u64 v[156:157], s[2:3], 0, v[4:5]
	s_movk_i32 s2, 0x7f80
	v_mov_b32_e32 v4, 0x6000
	v_cndmask_b32_e32 v8, 0, v8, vcc
	v_cmp_gt_i32_e32 vcc, s16, v14
	v_bitop3_b32 v4, v170, s2, v4 bitop3:0xc8
	v_ashrrev_i32_e32 v9, 31, v8
	v_cndmask_b32_e32 v14, 0, v14, vcc
	v_lshl_add_u64 v[160:161], s[18:19], 0, v[4:5]
	s_movk_i32 s2, 0xc000
	v_lshlrev_b64 v[8:9], 2, v[8:9]
	v_ashrrev_i32_e32 v15, 31, v14
	v_lshl_add_u64 v[4:5], v[160:161], 0, v[154:155]
	s_mov_b32 s3, -1
	v_lshl_add_u64 v[12:13], s[10:11], 0, v[8:9]
	v_lshlrev_b64 v[14:15], 2, v[14:15]
	v_add_u32_e32 v178, 0, v170
	v_lshl_add_u64 v[152:153], v[4:5], 0, s[2:3]
	v_lshl_add_u64 v[16:17], s[10:11], 0, v[14:15]
	global_load_dwordx4 v[70:73], v[12:13], off
	global_load_dwordx4 v[66:69], v[16:17], off
	v_readfirstlane_b32 s2, v178
	v_add_u32_e32 v12, 0x2000, v178
	s_mov_b32 m0, s2
	v_readfirstlane_b32 s2, v12
	v_add_u32_e32 v12, 0x4000, v178
	v_lshl_add_u64 v[150:151], v[156:157], 0, v[154:155]
	v_lshl_add_u64 v[158:159], s[18:19], 0, v[2:3]
	global_load_lds_dwordx4 v[146:147], off
	s_mov_b32 m0, s2
	v_readfirstlane_b32 s2, v12
	v_add_u32_e32 v12, 0x6000, v178
	v_lshl_add_u64 v[148:149], v[158:159], 0, v[154:155]
	global_load_lds_dwordx4 v[150:151], off
	s_mov_b32 m0, s2
	v_readfirstlane_b32 s2, v12
	v_add_u32_e32 v16, 0x8000, v178
	global_load_lds_dwordx4 v[148:149], off
	s_mov_b32 m0, s2
	s_mov_b64 s[10:11], 0x4000
	v_readfirstlane_b32 s2, v16
	v_add_u32_e32 v16, 0xa000, v178
	global_load_lds_dwordx4 v[152:153], off
	v_lshl_add_u64 v[12:13], v[146:147], 0, s[10:11]
	s_mov_b32 m0, s2
	v_readfirstlane_b32 s2, v16
	v_add_u32_e32 v16, 0xc000, v178
	global_load_lds_dwordx4 v[12:13], off
	v_lshl_add_u64 v[12:13], v[150:151], 0, s[10:11]
	s_mov_b32 m0, s2
	v_readfirstlane_b32 s2, v16
	global_load_lds_dwordx4 v[12:13], off
	v_lshl_add_u64 v[12:13], v[148:149], 0, s[10:11]
	s_mov_b32 m0, s2
	v_lshlrev_b32_e32 v169, 13, v19
	global_load_lds_dwordx4 v[12:13], off
	v_add_u32_e32 v12, 0xe000, v178
	s_nop 0
	v_readfirstlane_b32 s2, v12
	s_mov_b32 m0, s2
	s_add_i32 s2, 0, 0x10000
	v_add_u32_e32 v16, s2, v170
	s_mov_b64 s[2:3], 0x8000
	v_readfirstlane_b32 s14, v16
	v_add_u32_e32 v17, 0x2000, v16
	global_load_lds_dwordx4 v[4:5], off
	v_lshl_add_u64 v[12:13], v[146:147], 0, s[2:3]
	s_mov_b32 m0, s14
	v_readfirstlane_b32 s14, v17
	v_add_u32_e32 v17, 0x4000, v16
	global_load_lds_dwordx4 v[12:13], off
	v_lshl_add_u64 v[12:13], v[150:151], 0, s[2:3]
	s_mov_b32 m0, s14
	v_readfirstlane_b32 s14, v17
	global_load_lds_dwordx4 v[12:13], off
	v_lshl_add_u64 v[12:13], v[148:149], 0, s[2:3]
	s_mov_b32 m0, s14
	v_lshl_add_u64 v[4:5], v[4:5], 0, s[10:11]
	global_load_lds_dwordx4 v[12:13], off
	v_add_u32_e32 v12, 0x6000, v16
	s_mov_b32 s14, 0
	v_readfirstlane_b32 s10, v12
	s_mov_b32 m0, s10
	s_load_dwordx2 s[10:11], s[0:1], 0x38
	global_load_lds_dwordx4 v[4:5], off
	s_mov_b64 s[24:25], 0xc000
	v_add_u32_e32 v180, 0x18000, v170
	v_add_u32_e32 v181, 0x1a000, v170
	v_add_u32_e32 v182, 0x1c000, v170
	v_add_u32_e32 v183, 0x1e000, v170
	v_lshl_add_u64 v[12:13], v[146:147], 0, s[24:25]
	v_lshl_add_u64 v[16:17], v[150:151], 0, s[24:25]
	v_readfirstlane_b32 s26, v180
	v_readfirstlane_b32 s27, v181
	v_readfirstlane_b32 s28, v182
	v_readfirstlane_b32 s29, v183
	s_mov_b32 m0, s26
	v_lshl_add_u64 v[184:185], v[148:149], 0, s[24:25]
	global_load_lds_dwordx4 v[12:13], off
	s_mov_b32 m0, s27
	v_lshl_add_u64 v[186:187], v[152:153], 0, s[24:25]
	global_load_lds_dwordx4 v[16:17], off
	s_mov_b32 m0, s28
	s_nop 0
	global_load_lds_dwordx4 v[184:185], off
	s_mov_b32 m0, s29
	s_nop 0
	global_load_lds_dwordx4 v[186:187], off
	v_lshlrev_b32_e32 v4, 2, v168
	v_bfe_u32 v5, v0, 1, 3
	v_bitop3_b32 v4, v4, v5, v18 bitop3:0x36
	v_lshlrev_b32_e32 v22, 4, v4
	v_lshlrev_b32_e32 v4, 7, v164
	v_lshl_or_b32 v5, v1, 13, v4
	v_or_b32_e32 v24, v169, v4
	v_add_u32_e32 v171, v5, v22
	v_or_b32_e32 v5, 0x4000, v22
	v_or_b32_e32 v26, 0x1000, v24
	v_add_u32_e32 v23, 0x1000, v171
	v_add_u32_e32 v25, v5, v24
	v_add_u32_e32 v27, v5, v26
	s_waitcnt vmcnt(12)
	s_barrier
	v_add_u32_e32 v12, 0x800, v20
	s_movk_i32 s15, 0xfa0
	v_mov_b64_e32 v[4:5], s[12:13]
	v_mad_i64_i32 v[12:13], s[12:13], v12, s15, v[4:5]
	v_lshl_add_u64 v[16:17], v[12:13], 0, v[6:7]
	v_lshl_add_u64 v[18:19], v[12:13], 0, v[10:11]
	global_load_dwordx4 v[110:113], v[16:17], off
	global_load_dwordx4 v[106:109], v[18:19], off
	v_lshl_add_u64 v[16:17], v[12:13], 0, v[8:9]
	v_lshl_add_u64 v[12:13], v[12:13], 0, v[14:15]
	global_load_dwordx4 v[102:105], v[16:17], off
	global_load_dwordx4 v[98:101], v[12:13], off
	v_add_u32_e32 v12, 0x800, v21
	v_mad_i64_i32 v[4:5], s[12:13], v12, s15, v[4:5]
	v_lshl_add_u64 v[6:7], v[4:5], 0, v[6:7]
	v_lshl_add_u64 v[10:11], v[4:5], 0, v[10:11]
	global_load_dwordx4 v[94:97], v[6:7], off
	global_load_dwordx4 v[90:93], v[10:11], off
	v_lshl_add_u64 v[6:7], v[4:5], 0, v[8:9]
	v_lshl_add_u64 v[4:5], v[4:5], 0, v[14:15]
	global_load_dwordx4 v[86:89], v[6:7], off
	global_load_dwordx4 v[82:85], v[4:5], off
	v_add_u32_e32 v4, 0, v171
	v_add_u32_e32 v172, v22, v24
	ds_read_b128 v[130:133], v4
	ds_read_b128 v[126:129], v4 offset:4096
	v_add_u32_e32 v4, 0, v172
	v_add_u32_e32 v174, v22, v26
	v_xor_b32_e32 v177, 32, v171
	v_add_u32_e32 v5, 0, v174
	ds_read_b128 v[142:145], v4 offset:16384
	ds_read_b128 v[138:141], v5 offset:16384
	v_add_u32_e32 v4, 0, v177
	v_xor_b32_e32 v175, 32, v23
	v_xor_b32_e32 v173, 32, v25
	v_xor_b32_e32 v176, 32, v27
	v_add_u32_e32 v5, 0, v175
	v_add_u32_e32 v6, 0, v173
	v_add_u32_e32 v7, 0, v176
	ds_read_b128 v[134:137], v4
	ds_read_b128 v[114:117], v5
	ds_read_b128 v[122:125], v6
	ds_read_b128 v[118:121], v7
	s_cmpk_lt_i32 s8, 0x140
	s_cbranch_scc1 .LBB5_3
	s_ashr_i32 s12, s8, 31
	s_lshr_b32 s12, s12, 26
	s_add_i32 s8, s8, s12
	s_ashr_i32 s8, s8, 6
	s_add_i32 s8, s8, -4
	s_add_u32 s4, s4, s7
	s_addc_u32 s5, s5, s6
	v_lshl_add_u64 v[162:163], s[4:5], 0, v[2:3]
	s_mov_b64 s[24:25], 0x4000
	v_lshl_add_u64 v[162:163], v[162:163], 0, s[24:25]
	v_lshl_add_u64 v[156:157], v[156:157], 0, s[24:25]
	v_lshl_add_u64 v[158:159], v[158:159], 0, s[24:25]
	v_lshl_add_u64 v[160:161], v[160:161], 0, s[24:25]
	v_mov_b32_e32 v2, 0
	s_mov_b32 s12, 0x18000
	s_mov_b64 s[4:5], 0xc000
	s_mov_b64 s[6:7], 0x10000
	v_mov_b32_e32 v3, v2
	v_mov_b32_e32 v4, v2
	v_mov_b32_e32 v5, v2
	v_mov_b32_e32 v6, v2
	v_mov_b32_e32 v7, v2
	v_mov_b32_e32 v8, v2
	v_mov_b32_e32 v9, v2
	v_mov_b32_e32 v10, v2
	v_mov_b32_e32 v11, v2
	v_mov_b32_e32 v12, v2
	v_mov_b32_e32 v13, v2
	v_mov_b32_e32 v14, v2
	v_mov_b32_e32 v15, v2
	v_mov_b32_e32 v16, v2
	v_mov_b32_e32 v17, v2
	v_mov_b32_e32 v18, v2
	v_mov_b32_e32 v19, v2
	v_mov_b32_e32 v20, v2
	v_mov_b32_e32 v21, v2
	v_mov_b32_e32 v22, v2
	v_mov_b32_e32 v23, v2
	v_mov_b32_e32 v24, v2
	v_mov_b32_e32 v25, v2
	v_mov_b32_e32 v26, v2
	v_mov_b32_e32 v27, v2
	v_mov_b32_e32 v28, v2
	v_mov_b32_e32 v29, v2
	v_mov_b32_e32 v30, v2
	v_mov_b32_e32 v31, v2
	v_mov_b32_e32 v32, v2
	v_mov_b32_e32 v33, v2
	v_mov_b32_e32 v34, v2
	v_mov_b32_e32 v35, v2
	v_mov_b32_e32 v36, v2
	v_mov_b32_e32 v37, v2
	v_mov_b32_e32 v38, v2
	v_mov_b32_e32 v39, v2
	v_mov_b32_e32 v40, v2
	v_mov_b32_e32 v41, v2
	v_mov_b32_e32 v42, v2
	v_mov_b32_e32 v43, v2
	v_mov_b32_e32 v44, v2
	v_mov_b32_e32 v45, v2
	v_mov_b32_e32 v46, v2
	v_mov_b32_e32 v47, v2
	v_mov_b32_e32 v48, v2
	v_mov_b32_e32 v49, v2
	v_mov_b32_e32 v50, v2
	v_mov_b32_e32 v51, v2
	v_mov_b32_e32 v52, v2
	v_mov_b32_e32 v53, v2
	v_mov_b32_e32 v54, v2
	v_mov_b32_e32 v55, v2
	v_mov_b32_e32 v56, v2
	v_mov_b32_e32 v57, v2
	v_mov_b32_e32 v58, v2
	v_mov_b32_e32 v59, v2
	v_mov_b32_e32 v60, v2
	v_mov_b32_e32 v61, v2
	v_mov_b32_e32 v62, v2
	v_mov_b32_e32 v63, v2
	v_mov_b32_e32 v64, v2
	v_mov_b32_e32 v65, v2
.LBB5_2:
	s_waitcnt vmcnt(8) lgkmcnt(0)
	s_barrier
	v_mfma_f32_32x32x16_f16 v[50:65], v[130:133], v[142:145], v[50:65]
	s_add_i32 s13, s12, 0xfffe8000
	s_and_b32 s13, s13, 0x10000
	s_add_i32 s15, s13, 0
	s_add_i32 s26, s12, 0x8000
	s_and_b32 s26, s26, 0x18000
	v_add_u32_e32 v202, s26, v178
	v_lshl_add_u64 v[192:193], v[162:163], 0, v[154:155]
	v_add_u32_e32 v203, 0x2000, v202
	v_lshl_add_u64 v[200:201], v[192:193], 0, s[4:5]
	v_mfma_f32_32x32x16_f16 v[34:49], v[130:133], v[138:141], v[34:49]
	v_add_u32_e32 v130, s15, v171
	v_readfirstlane_b32 s26, v202
	v_readfirstlane_b32 s27, v203
	v_lshl_add_u64 v[194:195], v[156:157], 0, v[154:155]
	s_mov_b32 m0, s26
	v_add_u32_e32 v204, 0x4000, v202
	global_load_lds_dwordx4 v[200:201], off
	v_mfma_f32_32x32x16_f16 v[18:33], v[126:129], v[142:145], v[18:33]
	v_add_u32_e32 v142, s15, v177
	v_add_u32_e32 v143, s15, v175
	v_lshl_add_u64 v[200:201], v[194:195], 0, s[4:5]
	s_mov_b32 m0, s27
	v_readfirstlane_b32 s28, v204
	global_load_lds_dwordx4 v[200:201], off
	v_mfma_f32_32x32x16_f16 v[2:17], v[126:129], v[138:141], v[2:17]
	v_add_u32_e32 v138, s15, v174
	ds_read_b128 v[126:129], v130 offset:32768
	ds_read_b128 v[130:133], v130 offset:36864
	v_mfma_f32_32x32x16_f16 v[50:65], v[134:137], v[122:125], v[50:65]
	v_lshl_add_u64 v[196:197], v[158:159], 0, v[154:155]
	v_add_u32_e32 v205, 0x6000, v202
	v_lshl_add_u64 v[200:201], v[196:197], 0, s[4:5]
	s_mov_b32 m0, s28
	v_mfma_f32_32x32x16_f16 v[34:49], v[134:137], v[118:121], v[34:49]
	v_add_u32_e32 v134, s15, v172
	ds_read_b128 v[134:137], v134 offset:49152
	ds_read_b128 v[138:141], v138 offset:49152
	global_load_lds_dwordx4 v[200:201], off
	v_readfirstlane_b32 s29, v205
	v_mfma_f32_32x32x16_f16 v[18:33], v[114:117], v[122:125], v[18:33]
	ds_read_b128 v[122:125], v142 offset:32768
	ds_read_b128 v[180:183], v143 offset:32768
	v_add_u32_e32 v142, s15, v173
	v_add_u32_e32 v143, s15, v176
	ds_read_b128 v[184:187], v142 offset:32768
	ds_read_b128 v[188:191], v143 offset:32768
	v_lshl_add_u64 v[198:199], v[160:161], 0, v[154:155]
	v_lshl_add_u64 v[200:201], v[198:199], 0, s[2:3]
	s_mov_b32 m0, s29
	v_mfma_f32_32x32x16_f16 v[2:17], v[114:117], v[118:121], v[2:17]
	global_load_lds_dwordx4 v[200:201], off
	s_waitcnt vmcnt(8) lgkmcnt(0)
	s_barrier
	v_mfma_f32_32x32x16_f16 v[50:65], v[126:129], v[134:137], v[50:65]
	s_xor_b32 s15, s13, 0x10000
	s_add_i32 s15, s15, 0
	s_add_i32 s26, s13, 0x8000
	v_add_u32_e32 v202, s26, v178
	v_lshl_add_u64 v[200:201], v[192:193], 0, s[6:7]
	v_add_u32_e32 v114, s15, v171
	v_add_u32_e32 v115, s15, v174
	v_add_u32_e32 v118, s15, v173
	v_add_u32_e32 v119, s15, v176
	v_add_u32_e32 v203, 0x2000, v202
	v_readfirstlane_b32 s26, v202
	v_mfma_f32_32x32x16_f16 v[34:49], v[126:129], v[138:141], v[34:49]
	s_mov_b32 m0, s26
	v_readfirstlane_b32 s27, v203
	v_add_u32_e32 v204, 0x4000, v202
	global_load_lds_dwordx4 v[200:201], off
	v_mfma_f32_32x32x16_f16 v[18:33], v[130:133], v[134:137], v[18:33]
	v_lshl_add_u64 v[200:201], v[194:195], 0, s[6:7]
	s_mov_b32 m0, s27
	v_readfirstlane_b32 s28, v204
	global_load_lds_dwordx4 v[200:201], off
	v_mfma_f32_32x32x16_f16 v[2:17], v[130:133], v[138:141], v[2:17]
	ds_read_b128 v[130:133], v114
	ds_read_b128 v[126:129], v114 offset:4096
	v_add_u32_e32 v114, s15, v172
	ds_read_b128 v[142:145], v114 offset:16384
	ds_read_b128 v[138:141], v115 offset:16384
	v_add_u32_e32 v114, s15, v177
	v_add_u32_e32 v115, s15, v175
	ds_read_b128 v[134:137], v114
	ds_read_b128 v[114:117], v115
	v_mfma_f32_32x32x16_f16 v[50:65], v[122:125], v[184:187], v[50:65]
	v_lshl_add_u64 v[200:201], v[196:197], 0, s[6:7]
	v_add_u32_e32 v205, 0x6000, v202
	s_mov_b32 m0, s28
	v_mfma_f32_32x32x16_f16 v[34:49], v[122:125], v[188:191], v[34:49]
	ds_read_b128 v[122:125], v118
	ds_read_b128 v[118:121], v119
	global_load_lds_dwordx4 v[200:201], off
	v_readfirstlane_b32 s29, v205
	v_mfma_f32_32x32x16_f16 v[18:33], v[180:183], v[184:187], v[18:33]
	v_lshl_add_u64 v[200:201], v[198:199], 0, s[4:5]
	s_mov_b32 m0, s29
	v_mfma_f32_32x32x16_f16 v[2:17], v[180:183], v[188:191], v[2:17]
	global_load_lds_dwordx4 v[200:201], off
	s_add_i32 s14, s14, 2
	s_add_i32 s12, s12, 0x10000
	v_lshl_add_u64 v[162:163], v[162:163], 0, s[2:3]
	v_lshl_add_u64 v[156:157], v[156:157], 0, s[2:3]
	v_lshl_add_u64 v[158:159], v[158:159], 0, s[2:3]
	s_cmp_lt_i32 s14, s8
	v_lshl_add_u64 v[160:161], v[160:161], 0, s[2:3]
	s_cbranch_scc1 .LBB5_2
	s_branch .LBB5_4

.LBB5_4:
	v_lshrrev_b32_e32 v154, 6, v0
	v_and_b32_e32 v155, 63, v0
	s_waitcnt vmcnt(8) lgkmcnt(0)
	s_barrier
	v_mfma_f32_32x32x16_f16 v[50:65], v[130:133], v[142:145], v[50:65]
	s_lshl_b32 s4, s14, 15
	s_and_b32 s5, s4, 0x10000
	s_add_i32 s2, s5, 0
	v_add_u32_e32 v156, s2, v173
	v_add_u32_e32 v160, s2, v176
	s_mov_b32 s3, 0
	v_mfma_f32_32x32x16_f16 v[34:49], v[130:133], v[138:141], v[34:49]
	v_add_u32_e32 v130, s2, v171
	v_mfma_f32_32x32x16_f16 v[18:33], v[126:129], v[142:145], v[18:33]
	v_add_u32_e32 v142, s2, v177
	v_add_u32_e32 v143, s2, v175
	v_mfma_f32_32x32x16_f16 v[2:17], v[126:129], v[138:141], v[2:17]
	v_add_u32_e32 v138, s2, v174
	ds_read_b128 v[126:129], v130 offset:32768
	ds_read_b128 v[130:133], v130 offset:36864
	v_mfma_f32_32x32x16_f16 v[50:65], v[134:137], v[122:125], v[50:65]
	v_mfma_f32_32x32x16_f16 v[34:49], v[134:137], v[118:121], v[34:49]
	v_add_u32_e32 v134, s2, v172
	ds_read_b128 v[134:137], v134 offset:49152
	ds_read_b128 v[138:141], v138 offset:49152
	v_mfma_f32_32x32x16_f16 v[18:33], v[114:117], v[122:125], v[18:33]
	ds_read_b128 v[122:125], v142 offset:32768
	ds_read_b128 v[142:145], v143 offset:32768
	ds_read_b128 v[156:159], v156 offset:32768
	ds_read_b128 v[160:163], v160 offset:32768
	v_mfma_f32_32x32x16_f16 v[2:17], v[114:117], v[118:121], v[2:17]
	s_waitcnt vmcnt(4) lgkmcnt(0)
	s_barrier
	v_mfma_f32_32x32x16_f16 v[50:65], v[126:129], v[134:137], v[50:65]
	s_xor_b32 s2, s5, 0x10000
	s_add_i32 s2, s2, 0
	v_add_u32_e32 v118, s2, v171
	v_add_u32_e32 v146, s2, v176
	ds_read_b128 v[114:117], v118
	ds_read_b128 v[118:121], v118 offset:4096
	v_mfma_f32_32x32x16_f16 v[34:49], v[126:129], v[138:141], v[34:49]
	v_add_u32_e32 v126, s2, v174
	v_mfma_f32_32x32x16_f16 v[18:33], v[130:133], v[134:137], v[18:33]
	v_add_u32_e32 v134, s2, v175
	v_mfma_f32_32x32x16_f16 v[2:17], v[130:133], v[138:141], v[2:17]
	v_add_u32_e32 v130, s2, v177
	v_add_u32_e32 v138, s2, v173
	v_mfma_f32_32x32x16_f16 v[50:65], v[122:125], v[156:159], v[50:65]
	v_mfma_f32_32x32x16_f16 v[34:49], v[122:125], v[160:163], v[34:49]
	v_add_u32_e32 v122, s2, v172
	ds_read_b128 v[122:125], v122 offset:16384
	ds_read_b128 v[126:129], v126 offset:16384
	ds_read_b128 v[130:133], v130
	ds_read_b128 v[134:137], v134
	ds_read_b128 v[138:141], v138
	ds_read_b128 v[146:149], v146
	v_mfma_f32_32x32x16_f16 v[18:33], v[142:145], v[156:159], v[18:33]
	v_mfma_f32_32x32x16_f16 v[2:17], v[142:145], v[160:163], v[2:17]
	s_waitcnt vmcnt(0) lgkmcnt(0)
	s_barrier
	v_mfma_f32_32x32x16_f16 v[50:65], v[114:117], v[122:125], v[50:65]
	s_add_i32 s4, s4, 0x18000
	s_and_b32 s2, s4, 0x18000
	s_add_i32 s2, s2, 0
	v_add_u32_e32 v142, s2, v173
	v_add_u32_e32 v150, s2, v176
	v_mfma_f32_32x32x16_f16 v[34:49], v[114:117], v[126:129], v[34:49]
	v_mfma_f32_32x32x16_f16 v[18:33], v[118:121], v[122:125], v[18:33]
	v_add_u32_e32 v122, s2, v172
	v_mfma_f32_32x32x16_f16 v[2:17], v[118:121], v[126:129], v[2:17]
	v_add_u32_e32 v118, s2, v171
	v_add_u32_e32 v126, s2, v174
	ds_read_b128 v[114:117], v118
	ds_read_b128 v[118:121], v118 offset:4096
	ds_read_b128 v[122:125], v122 offset:16384
	ds_read_b128 v[126:129], v126 offset:16384
	v_mfma_f32_32x32x16_f16 v[50:65], v[130:133], v[138:141], v[50:65]
	v_mfma_f32_32x32x16_f16 v[34:49], v[130:133], v[146:149], v[34:49]
	v_add_u32_e32 v130, s2, v177
	v_mfma_f32_32x32x16_f16 v[18:33], v[134:137], v[138:141], v[18:33]
	v_add_u32_e32 v138, s2, v175
	ds_read_b128 v[130:133], v130
	ds_read_b128 v[138:141], v138
	ds_read_b128 v[142:145], v142
	ds_read_b128 v[150:153], v150
	v_mfma_f32_32x32x16_f16 v[2:17], v[134:137], v[146:149], v[2:17]
	s_waitcnt vmcnt(0) lgkmcnt(0)
	s_barrier
	v_mfma_f32_32x32x16_f16 v[50:65], v[114:117], v[122:125], v[50:65]
	v_mfma_f32_32x32x16_f16 v[34:49], v[114:117], v[126:129], v[34:49]
	v_mfma_f32_32x32x16_f16 v[18:33], v[118:121], v[122:125], v[18:33]
	v_mfma_f32_32x32x16_f16 v[2:17], v[118:121], v[126:129], v[2:17]
	v_mfma_f32_32x32x16_f16 v[50:65], v[130:133], v[142:145], v[50:65]
	v_mfma_f32_32x32x16_f16 v[34:49], v[130:133], v[150:153], v[34:49]
	v_mfma_f32_32x32x16_f16 v[18:33], v[138:141], v[142:145], v[18:33]
	v_mfma_f32_32x32x16_f16 v[2:17], v[138:141], v[150:153], v[2:17]
	s_waitcnt vmcnt(0) lgkmcnt(0)
	s_movk_i32 s2, 0x100
	s_movk_i32 s4, 0xff
	v_lshl_add_u32 v114, v155, 2, 0
	v_cmp_gt_u32_e64 s[2:3], s2, v0
	v_cmp_lt_u32_e32 vcc, s4, v0
	v_lshlrev_b32_e32 v0, 14, v1
	s_barrier
	s_and_saveexec_b64 s[4:5], vcc
	s_cbranch_execz .LBB5_6
	v_add3_u32 v1, v114, v0, v169
	ds_write2st64_b32 v1, v50, v51 offset1:1
	ds_write2st64_b32 v1, v52, v53 offset0:2 offset1:3
	ds_write2st64_b32 v1, v54, v55 offset0:4 offset1:5
	ds_write2st64_b32 v1, v56, v57 offset0:6 offset1:7
	ds_write2st64_b32 v1, v58, v59 offset0:8 offset1:9
	ds_write2st64_b32 v1, v60, v61 offset0:10 offset1:11
	ds_write2st64_b32 v1, v62, v63 offset0:12 offset1:13
	ds_write2st64_b32 v1, v64, v65 offset0:14 offset1:15
	ds_write2st64_b32 v1, v34, v35 offset0:16 offset1:17
	ds_write2st64_b32 v1, v36, v37 offset0:18 offset1:19
	ds_write2st64_b32 v1, v38, v39 offset0:20 offset1:21
	ds_write2st64_b32 v1, v40, v41 offset0:22 offset1:23
	ds_write2st64_b32 v1, v42, v43 offset0:24 offset1:25
	ds_write2st64_b32 v1, v44, v45 offset0:26 offset1:27
	ds_write2st64_b32 v1, v46, v47 offset0:28 offset1:29
	ds_write2st64_b32 v1, v48, v49 offset0:30 offset1:31

.LBB5_44:
	s_or_b64 exec, exec, s[0:1]
	v_perm_b32 v0, v0, v4, s2
	v_lshl_add_u64 v[2:3], v[2:3], 0, v[22:23]
	global_store_dwordx2 v[2:3], v[0:1], off
	s_endpgm
	.p2align 8

	.amdhsa_kernel _Z7gemm_x3ILi2ELi2ELi2ELi0EEvPKcS1_iiPKfiS3_PKiPciPy
		.amdhsa_group_segment_fixed_size 0
		.amdhsa_private_segment_fixed_size 0
		.amdhsa_kernarg_size 80
		.amdhsa_user_sgpr_count 2
		.amdhsa_user_sgpr_dispatch_ptr 0
		.amdhsa_user_sgpr_queue_ptr 0
		.amdhsa_user_sgpr_kernarg_segment_ptr 1
		.amdhsa_user_sgpr_dispatch_id 0
		.amdhsa_user_sgpr_kernarg_preload_length 0
		.amdhsa_user_sgpr_kernarg_preload_offset 0
		.amdhsa_user_sgpr_private_segment_size 0
		.amdhsa_uses_dynamic_stack 0
		.amdhsa_enable_private_segment 0
		.amdhsa_system_sgpr_workgroup_id_x 1
		.amdhsa_system_sgpr_workgroup_id_y 0
		.amdhsa_system_sgpr_workgroup_id_z 0
		.amdhsa_system_sgpr_workgroup_info 0
		.amdhsa_system_vgpr_workitem_id 0
		.amdhsa_next_free_vgpr 208
		.amdhsa_next_free_sgpr 32
		.amdhsa_accum_offset 208
		.amdhsa_reserve_vcc 1
		.amdhsa_float_round_mode_32 0
		.amdhsa_float_round_mode_16_64 0
		.amdhsa_float_denorm_mode_32 3
		.amdhsa_float_denorm_mode_16_64 3
		.amdhsa_dx10_clamp 1
		.amdhsa_ieee_mode 1
		.amdhsa_fp16_overflow 0
		.amdhsa_tg_split 0
		.amdhsa_exception_fp_ieee_invalid_op 0
		.amdhsa_exception_fp_denorm_src 0
		.amdhsa_exception_fp_ieee_div_zero 0
		.amdhsa_exception_fp_ieee_overflow 0
		.amdhsa_exception_fp_ieee_underflow 0
		.amdhsa_exception_fp_ieee_inexact 0
		.amdhsa_exception_int_div_zero 0
	.end_amdhsa_kernel

.LBB6_28:
	s_or_b64 exec, exec, s[0:1]
	v_perm_b32 v2, v2, v4, s2
	v_lshlrev_b32_e32 v4, 1, v5
	v_ashrrev_i32_e32 v5, 31, v4
	v_lshl_add_u64 v[0:1], v[0:1], 0, v[4:5]
	global_store_dwordx2 v[0:1], v[2:3], off
	s_endpgm
	.p2align 8

_Z13refine_kernelILi1ELi16ELi128ELb1ELi4EEvPKfiiS1_iiS1_PKiS3_S3_PfiPy:
	s_cmpk_gt_i32 s3, 0xff
	s_movk_i32 s4, 0xff
	s_cbranch_scc1 .LBB8_11
	s_load_dwordx8 s[12:19], s[0:1], 0x0
	s_load_dwordx8 s[20:27], s[0:1], 0x20
	s_load_dwordx2 s[10:11], s[0:1], 0x40
	s_load_dword s28, s[0:1], 0x48
	v_and_b32_e32 v28, 15, v0
	v_lshl_or_b32 v2, s2, 4, v28
	s_waitcnt lgkmcnt(0)
	v_cmp_le_i32_e64 s[6:7], s19, v2
	s_load_dword s2, s[26:27], 0x0
	v_lshrrev_b32_e32 v1, 2, v0
	v_cndmask_b32_e64 v4, v2, 0, s[6:7]
	v_ashrrev_i32_e32 v5, 31, v4
	s_add_i32 s19, s19, -1
	v_lshl_add_u64 v[12:13], v[4:5], 2, s[16:17]
	v_and_b32_e32 v1, 12, v1
	v_lshrrev_b32_e32 v3, 6, v0
	v_and_b32_e32 v6, 63, v0
	v_min_i32_e32 v4, s19, v2
	v_and_or_b32 v29, v3, 3, v1
	v_ashrrev_i32_e32 v5, 31, v4
	s_ashr_i32 s19, s18, 31
	v_lshl_or_b32 v30, v3, 7, v1
	v_lshlrev_b32_e32 v1, 2, v6
	v_cmp_lt_u32_e64 s[8:9], s4, v0
	s_movk_i32 s4, 0x100
	v_lshlrev_b64 v[4:5], 2, v[4:5]
	v_lshl_or_b32 v31, v3, 10, v1
	v_ashrrev_i32_e32 v3, 31, v2
	s_add_u32 s0, s0, 0x58
	v_cmp_gt_u32_e64 s[4:5], s4, v0
	v_lshl_add_u64 v[14:15], s[20:21], 0, v[4:5]
	v_lshl_add_u64 v[16:17], s[16:17], 0, v[4:5]
	v_lshl_add_u64 v[18:19], v[2:3], 2, s[10:11]
	s_addc_u32 s1, s1, 0
	v_mov_b32_e32 v21, 0
	s_branch .LBB8_4

.LBB8_4:
	s_lshl_b32 s16, s3, 4
	s_waitcnt lgkmcnt(0)
	s_cmp_ge_i32 s16, s2
	s_cbranch_scc1 .LBB8_11
	s_waitcnt vmcnt(0)
	v_or_b32_e32 v0, s16, v28
	v_ashrrev_i32_e32 v1, 31, v0
	v_lshl_add_u64 v[0:1], v[0:1], 2, s[24:25]
	global_load_dword v0, v[0:1], off
	v_or_b32_e32 v22, s16, v29
	v_mov_b32_e32 v23, v21
	s_and_saveexec_b64 s[10:11], s[4:5]
	s_cbranch_execnz .LBB8_6
	s_or_b64 exec, exec, s[10:11]
	s_waitcnt lgkmcnt(0)
	s_cmp_ge_i32 s16, s2
	s_mov_b64 s[10:11], -1
	s_cbranch_scc1 .LBB8_3
	s_branch .LBB8_7

.LBB8_8:
	v_or_b32_e32 v20, s16, v30
	v_mad_u64_u32 v[4:5], s[16:17], v20, s18, 0
	v_mov_b32_e32 v6, v5
	v_mad_u64_u32 v[6:7], s[16:17], v20, s19, v[6:7]
	v_or_b32_e32 v33, 16, v20
	v_mov_b32_e32 v5, v6
	v_or_b32_e32 v7, 1, v20
	v_mad_u64_u32 v[42:43], s[16:17], v33, s18, 0
	v_lshl_add_u64 v[34:35], v[4:5], 2, v[12:13]
	v_mad_u64_u32 v[4:5], s[16:17], v7, s18, 0
	v_mov_b32_e32 v44, v43
	v_mov_b32_e32 v6, v5
	v_mad_u64_u32 v[44:45], s[16:17], v33, s19, v[44:45]
	v_or_b32_e32 v33, 17, v20
	v_mad_u64_u32 v[6:7], s[16:17], v7, s19, v[6:7]
	v_mov_b32_e32 v43, v44
	v_mad_u64_u32 v[44:45], s[16:17], v33, s18, 0
	v_mov_b32_e32 v5, v6
	v_or_b32_e32 v7, 2, v20
	v_mov_b32_e32 v46, v45
	v_lshl_add_u64 v[36:37], v[4:5], 2, v[12:13]
	v_mad_u64_u32 v[4:5], s[16:17], v7, s18, 0
	v_mad_u64_u32 v[46:47], s[16:17], v33, s19, v[46:47]
	v_or_b32_e32 v33, 18, v20
	v_mov_b32_e32 v6, v5
	v_mov_b32_e32 v45, v46
	v_mad_u64_u32 v[46:47], s[16:17], v33, s18, 0
	v_mad_u64_u32 v[6:7], s[16:17], v7, s19, v[6:7]
	v_mov_b32_e32 v48, v47
	v_mov_b32_e32 v5, v6
	v_or_b32_e32 v7, 3, v20
	v_mad_u64_u32 v[48:49], s[16:17], v33, s19, v[48:49]
	v_or_b32_e32 v33, 19, v20
	v_lshl_add_u64 v[38:39], v[4:5], 2, v[12:13]
	v_mad_u64_u32 v[4:5], s[16:17], v7, s18, 0
	v_mov_b32_e32 v47, v48
	v_mad_u64_u32 v[48:49], s[16:17], v33, s18, 0
	v_mov_b32_e32 v6, v5
	v_mov_b32_e32 v50, v49
	v_mad_u64_u32 v[6:7], s[16:17], v7, s19, v[6:7]
	v_mad_u64_u32 v[50:51], s[16:17], v33, s19, v[50:51]
	v_lshl_add_u64 v[26:27], v[20:21], 2, v[24:25]
	v_mov_b32_e32 v5, v6
	v_mov_b32_e32 v49, v50
	v_lshl_add_u64 v[40:41], v[4:5], 2, v[12:13]
	global_load_dwordx4 v[8:11], v[26:27], off
	global_load_dwordx4 v[4:7], v[26:27], off offset:64
	v_lshl_add_u64 v[42:43], v[42:43], 2, v[12:13]
	v_lshl_add_u64 v[44:45], v[44:45], 2, v[12:13]
	v_lshl_add_u64 v[46:47], v[46:47], 2, v[12:13]
	v_lshl_add_u64 v[48:49], v[48:49], 2, v[12:13]
	global_load_dword v33, v[34:35], off
	global_load_dword v58, v[36:37], off
	global_load_dword v59, v[38:39], off
	global_load_dword v60, v[40:41], off
	global_load_dword v61, v[42:43], off
	global_load_dword v62, v[44:45], off
	global_load_dword v63, v[46:47], off
	global_load_dword v32, v[48:49], off
	v_or_b32_e32 v37, 32, v20
	v_mad_u64_u32 v[34:35], s[16:17], v37, s18, 0
	v_mov_b32_e32 v36, v35
	v_mad_u64_u32 v[36:37], s[16:17], v37, s19, v[36:37]
	v_mov_b32_e32 v35, v36
	v_or_b32_e32 v37, 33, v20
	v_lshl_add_u64 v[42:43], v[34:35], 2, v[12:13]
	v_mad_u64_u32 v[34:35], s[16:17], v37, s18, 0
	v_mov_b32_e32 v36, v35
	v_mad_u64_u32 v[36:37], s[16:17], v37, s19, v[36:37]
	v_mov_b32_e32 v35, v36
	v_or_b32_e32 v37, 34, v20
	v_lshl_add_u64 v[44:45], v[34:35], 2, v[12:13]
	v_mad_u64_u32 v[34:35], s[16:17], v37, s18, 0
	v_mov_b32_e32 v36, v35
	v_mad_u64_u32 v[36:37], s[16:17], v37, s19, v[36:37]
	v_mov_b32_e32 v35, v36
	v_or_b32_e32 v37, 35, v20
	v_lshl_add_u64 v[46:47], v[34:35], 2, v[12:13]
	v_mad_u64_u32 v[34:35], s[16:17], v37, s18, 0
	v_mov_b32_e32 v36, v35
	v_mad_u64_u32 v[36:37], s[16:17], v37, s19, v[36:37]
	v_mov_b32_e32 v35, v36
	v_or_b32_e32 v51, 48, v20
	v_lshl_add_u64 v[48:49], v[34:35], 2, v[12:13]
	global_load_dwordx4 v[34:37], v[26:27], off offset:128
	global_load_dwordx4 v[38:41], v[26:27], off offset:192
	v_mad_u64_u32 v[26:27], s[16:17], v51, s18, 0
	v_mov_b32_e32 v50, v27
	v_mad_u64_u32 v[50:51], s[16:17], v51, s19, v[50:51]
	v_or_b32_e32 v53, 49, v20
	v_mov_b32_e32 v27, v50
	v_mad_u64_u32 v[50:51], s[16:17], v53, s18, 0
	v_mov_b32_e32 v52, v51
	v_mad_u64_u32 v[52:53], s[16:17], v53, s19, v[52:53]
	v_or_b32_e32 v55, 50, v20
	v_mov_b32_e32 v51, v52
	v_mad_u64_u32 v[52:53], s[16:17], v55, s18, 0
	v_mov_b32_e32 v54, v53
	v_mad_u64_u32 v[54:55], s[16:17], v55, s19, v[54:55]
	v_or_b32_e32 v56, 51, v20
	v_mov_b32_e32 v53, v54
	v_mad_u64_u32 v[54:55], s[16:17], v56, s18, 0
	v_mov_b32_e32 v20, v55
	v_mad_u64_u32 v[56:57], s[16:17], v56, s19, v[20:21]
	v_mov_b32_e32 v55, v56
	v_lshl_add_u64 v[26:27], v[26:27], 2, v[12:13]
	v_lshl_add_u64 v[50:51], v[50:51], 2, v[12:13]
	v_lshl_add_u64 v[52:53], v[52:53], 2, v[12:13]
	v_lshl_add_u64 v[54:55], v[54:55], 2, v[12:13]
	global_load_dword v20, v[42:43], off
	s_nop 0
	global_load_dword v42, v[44:45], off
	global_load_dword v43, v[46:47], off
	global_load_dword v56, v[48:49], off
	s_nop 0
	global_load_dword v44, v[26:27], off
	global_load_dword v45, v[50:51], off
	global_load_dword v46, v[52:53], off
	global_load_dword v47, v[54:55], off
	v_cndmask_b32_e64 v26, 0, 1, s[10:11]
	v_cmp_ne_u32_e32 vcc, 1, v26
	s_waitcnt vmcnt(17)
	v_mfma_f32_16x16x4_f32 v[0:3], v8, v33, v[0:3]
	s_mov_b32 s16, 64
	s_mov_b64 s[10:11], 0
	s_and_b64 vcc, exec, vcc
	s_waitcnt vmcnt(16)
	v_mfma_f32_16x16x4_f32 v[0:3], v9, v58, v[0:3]
	s_waitcnt vmcnt(15)
	v_mfma_f32_16x16x4_f32 v[0:3], v10, v59, v[0:3]
	s_waitcnt vmcnt(14)
	v_mfma_f32_16x16x4_f32 v[0:3], v11, v60, v[0:3]
	s_waitcnt vmcnt(13)
	v_mfma_f32_16x16x4_f32 v[0:3], v4, v61, v[0:3]
	s_waitcnt vmcnt(12)
	v_mfma_f32_16x16x4_f32 v[0:3], v5, v62, v[0:3]
	s_waitcnt vmcnt(11)
	v_mfma_f32_16x16x4_f32 v[0:3], v6, v63, v[0:3]
	s_waitcnt vmcnt(10)
	v_mfma_f32_16x16x4_f32 v[0:3], v7, v32, v[0:3]
	s_waitcnt vmcnt(7)
	v_mfma_f32_16x16x4_f32 v[0:3], v34, v20, v[0:3]
	s_waitcnt vmcnt(6)
	v_mfma_f32_16x16x4_f32 v[0:3], v35, v42, v[0:3]
	s_waitcnt vmcnt(5)
	v_mfma_f32_16x16x4_f32 v[0:3], v36, v43, v[0:3]
	s_waitcnt vmcnt(4)
	v_mfma_f32_16x16x4_f32 v[0:3], v37, v56, v[0:3]
	s_waitcnt vmcnt(3)
	v_mfma_f32_16x16x4_f32 v[0:3], v38, v44, v[0:3]
	s_waitcnt vmcnt(2)
	v_mfma_f32_16x16x4_f32 v[0:3], v39, v45, v[0:3]
	s_waitcnt vmcnt(1)
	v_mfma_f32_16x16x4_f32 v[0:3], v40, v46, v[0:3]
	s_waitcnt vmcnt(0)
	v_mfma_f32_16x16x4_f32 v[0:3], v41, v47, v[0:3]
	s_cbranch_vccz .LBB8_8
	v_cmp_le_i32_e32 vcc, s2, v22
	s_or_b64 s[10:11], s[8:9], vcc
	s_nor_b64 s[16:17], s[10:11], s[6:7]
	s_nop 5
	ds_write2st64_b32 v31, v0, v1 offset1:1
	ds_write2st64_b32 v31, v2, v3 offset0:2 offset1:3
	s_waitcnt lgkmcnt(0)
	s_barrier
	s_and_saveexec_b64 s[10:11], s[16:17]
	s_cbranch_execz .LBB8_2
	v_lshrrev_b32_e32 v32, 10, v31
	v_mul_u32_u24_e32 v32, 0x300, v32
	v_sub_u32_e32 v32, v31, v32
	ds_read2st64_b32 v[0:1], v32 offset1:4
	ds_read2st64_b32 v[2:3], v32 offset0:8 offset1:12
	ds_read2st64_b32 v[4:5], v32 offset0:16 offset1:20
	ds_read2st64_b32 v[6:7], v32 offset0:24 offset1:28
	ds_read2st64_b32 v[8:9], v32 offset0:32 offset1:36
	s_waitcnt lgkmcnt(4)
	v_add_f32_e32 v0, 0, v0
	v_add_f32_e32 v0, v0, v1
	s_waitcnt lgkmcnt(3)
	v_add_f32_e32 v0, v0, v2
	v_add_f32_e32 v0, v0, v3
	s_waitcnt lgkmcnt(2)
	v_add_f32_e32 v0, v0, v4
	v_add_f32_e32 v0, v0, v5
	s_waitcnt lgkmcnt(1)
	v_add_f32_e32 v0, v0, v6
	v_add_f32_e32 v2, v0, v7
	ds_read2st64_b32 v[0:1], v32 offset0:40 offset1:44
	s_waitcnt lgkmcnt(1)
	v_add_f32_e32 v4, v2, v8
	ds_read2st64_b32 v[2:3], v32 offset0:48 offset1:52
	v_add_f32_e32 v6, v4, v9
	ds_read2st64_b32 v[4:5], v32 offset0:56 offset1:60
	s_waitcnt lgkmcnt(2)
	v_add_f32_e32 v0, v6, v0
	v_add_f32_e32 v0, v0, v1
	s_waitcnt lgkmcnt(1)
	v_add_f32_e32 v0, v0, v2
	v_add_f32_e32 v0, v0, v3
	s_waitcnt lgkmcnt(0)
	v_add_f32_e32 v0, v0, v4
	v_add_f32_e32 v0, v0, v5
	v_add_f32_e32 v0, v23, v0
	v_max_f32_e32 v2, 0, v0
	v_mad_i64_i32 v[0:1], s[16:17], v22, s28, 0
	v_lshl_add_u64 v[0:1], v[0:1], 2, v[18:19]
	global_store_dword v[0:1], v2, off
	s_branch .LBB8_2

	.amdhsa_kernel _Z13refine_kernelILi1ELi16ELi128ELb1ELi4EEvPKfiiS1_iiS1_PKiS3_S3_PfiPy
		.amdhsa_group_segment_fixed_size 16384
		.amdhsa_private_segment_fixed_size 0
		.amdhsa_kernarg_size 344
		.amdhsa_user_sgpr_count 2
		.amdhsa_user_sgpr_dispatch_ptr 0
		.amdhsa_user_sgpr_queue_ptr 0
		.amdhsa_user_sgpr_kernarg_segment_ptr 1
		.amdhsa_user_sgpr_dispatch_id 0
		.amdhsa_user_sgpr_kernarg_preload_length 0
		.amdhsa_user_sgpr_kernarg_preload_offset 0
		.amdhsa_user_sgpr_private_segment_size 0
		.amdhsa_uses_dynamic_stack 0
		.amdhsa_enable_private_segment 0
		.amdhsa_system_sgpr_workgroup_id_x 1
		.amdhsa_system_sgpr_workgroup_id_y 1
		.amdhsa_system_sgpr_workgroup_id_z 0
		.amdhsa_system_sgpr_workgroup_info 0
		.amdhsa_system_vgpr_workitem_id 0
		.amdhsa_next_free_vgpr 64
		.amdhsa_next_free_sgpr 29
		.amdhsa_accum_offset 64
		.amdhsa_reserve_vcc 1
		.amdhsa_float_round_mode_32 0
		.amdhsa_float_round_mode_16_64 0
		.amdhsa_float_denorm_mode_32 3
		.amdhsa_float_denorm_mode_16_64 3
		.amdhsa_dx10_clamp 1
		.amdhsa_ieee_mode 1
		.amdhsa_fp16_overflow 0
		.amdhsa_tg_split 0
		.amdhsa_exception_fp_ieee_invalid_op 0
		.amdhsa_exception_fp_denorm_src 0
		.amdhsa_exception_fp_ieee_div_zero 0
		.amdhsa_exception_fp_ieee_overflow 0
		.amdhsa_exception_fp_ieee_underflow 0
		.amdhsa_exception_fp_ieee_inexact 0
		.amdhsa_exception_int_div_zero 0
	.end_amdhsa_kernel

amdhsa.kernels:
  - .agpr_count:     0
    .args:
      - .actual_access:  read_only
        .address_space:  global
        .offset:         0
        .size:           8
        .value_kind:     global_buffer
      - .actual_access:  write_only
        .address_space:  global
        .offset:         8
        .size:           8
        .value_kind:     global_buffer
      - .actual_access:  read_only
        .address_space:  global
        .offset:         16
        .size:           8
        .value_kind:     global_buffer
      - .actual_access:  read_only
        .address_space:  global
        .offset:         24
        .size:           8
        .value_kind:     global_buffer
      - .actual_access:  read_only
        .address_space:  global
        .offset:         32
        .size:           8
        .value_kind:     global_buffer
      - .actual_access:  write_only
        .address_space:  global
        .offset:         40
        .size:           8
        .value_kind:     global_buffer
      - .actual_access:  write_only
        .address_space:  global
        .offset:         48
        .size:           8
        .value_kind:     global_buffer
      - .actual_access:  write_only
        .address_space:  global
        .offset:         56
        .size:           8
        .value_kind:     global_buffer
      - .actual_access:  write_only
        .address_space:  global
        .offset:         64
        .size:           8
        .value_kind:     global_buffer
      - .actual_access:  write_only
        .address_space:  global
        .offset:         72
        .size:           8
        .value_kind:     global_buffer
      - .actual_access:  write_only
        .address_space:  global
        .offset:         80
        .size:           8
        .value_kind:     global_buffer
    .group_segment_fixed_size: 16640
    .kernarg_segment_align: 8
    .kernarg_segment_size: 88
    .language:       OpenCL C
    .language_version:
      - 2
      - 0
    .max_flat_workgroup_size: 256
    .name:           _Z8prep_allPKfPcS0_S0_S0_S1_S1_S1_PyPiS3_
    .private_segment_fixed_size: 0
    .sgpr_count:     30
    .sgpr_spill_count: 0
    .symbol:         _Z8prep_allPKfPcS0_S0_S0_S1_S1_S1_PyPiS3_.kd
    .uniform_work_group_size: 1
    .uses_dynamic_stack: false
    .vgpr_count:     48
    .vgpr_spill_count: 0
    .wavefront_size: 64
  - .agpr_count:     0
    .args:
      - .actual_access:  read_only
        .address_space:  global
        .offset:         0
        .size:           8
        .value_kind:     global_buffer
      - .actual_access:  write_only
        .address_space:  global
        .offset:         8
        .size:           8
        .value_kind:     global_buffer
      - .actual_access:  write_only
        .address_space:  global
        .offset:         16
        .size:           8
        .value_kind:     global_buffer
      - .address_space:  global
        .offset:         24
        .size:           8
        .value_kind:     global_buffer
    .group_segment_fixed_size: 0
    .kernarg_segment_align: 8
    .kernarg_segment_size: 32
    .language:       OpenCL C
    .language_version:
      - 2
      - 0
    .max_flat_workgroup_size: 256
    .name:           _Z13select_kernelPKfPyPiS2_
    .private_segment_fixed_size: 0
    .sgpr_count:     21
    .sgpr_spill_count: 0
    .symbol:         _Z13select_kernelPKfPyPiS2_.kd
    .uniform_work_group_size: 1
    .uses_dynamic_stack: false
    .vgpr_count:     12
    .vgpr_spill_count: 0
    .wavefront_size: 64
  - .agpr_count:     0
    .args:
      - .actual_access:  read_only
        .address_space:  global
        .offset:         0
        .size:           8
        .value_kind:     global_buffer
      - .actual_access:  write_only
        .address_space:  global
        .offset:         8
        .size:           8
        .value_kind:     global_buffer
      - .actual_access:  write_only
        .address_space:  global
        .offset:         16
        .size:           8
        .value_kind:     global_buffer
      - .actual_access:  write_only
        .address_space:  global
        .offset:         24
        .size:           8
        .value_kind:     global_buffer
    .group_segment_fixed_size: 4128
    .kernarg_segment_align: 8
    .kernarg_segment_size: 32
    .language:       OpenCL C
    .language_version:
      - 2
      - 0
    .max_flat_workgroup_size: 1024
    .name:           _Z12route_kernelPKyPiP15HIP_vector_typeIiLj4EES1_
    .private_segment_fixed_size: 0
    .sgpr_count:     19
    .sgpr_spill_count: 0
    .symbol:         _Z12route_kernelPKyPiP15HIP_vector_typeIiLj4EES1_.kd
    .uniform_work_group_size: 1
    .uses_dynamic_stack: false
    .vgpr_count:     23
    .vgpr_spill_count: 0
    .wavefront_size: 64
  - .agpr_count:     66
    .args:
      - .actual_access:  read_only
        .address_space:  global
        .offset:         0
        .size:           8
        .value_kind:     global_buffer
      - .actual_access:  read_only
        .address_space:  global
        .offset:         8
        .size:           8
        .value_kind:     global_buffer
      - .actual_access:  read_only
        .address_space:  global
        .offset:         16
        .size:           8
        .value_kind:     global_buffer
      - .actual_access:  read_only
        .address_space:  global
        .offset:         24
        .size:           8
        .value_kind:     global_buffer
      - .actual_access:  read_only
        .address_space:  global
        .offset:         32
        .size:           8
        .value_kind:     global_buffer
      - .actual_access:  write_only
        .address_space:  global
        .offset:         40
        .size:           8
        .value_kind:     global_buffer
    .group_segment_fixed_size: 51200
    .kernarg_segment_align: 8
    .kernarg_segment_size: 48
    .language:       OpenCL C
    .language_version:
      - 2
      - 0
    .max_flat_workgroup_size: 256
    .name:           _Z13expert_kernelPKcPKfPKiPK15HIP_vector_typeIiLj4EES4_Pf
    .private_segment_fixed_size: 0
    .sgpr_count:     20
    .sgpr_spill_count: 0
    .symbol:         _Z13expert_kernelPKcPKfPKiPK15HIP_vector_typeIiLj4EES4_Pf.kd
    .uniform_work_group_size: 1
    .uses_dynamic_stack: false
    .vgpr_count:     154
    .vgpr_spill_count: 0
    .wavefront_size: 64
  - .agpr_count:     0
    .args:
      - .actual_access:  read_only
        .address_space:  global
        .offset:         0
        .size:           8
        .value_kind:     global_buffer
      - .actual_access:  read_only
        .address_space:  global
        .offset:         8
        .size:           8
        .value_kind:     global_buffer
      - .actual_access:  read_only
        .address_space:  global
        .offset:         16
        .size:           8
        .value_kind:     global_buffer
      - .actual_access:  read_only
        .address_space:  global
        .offset:         24
        .size:           8
        .value_kind:     global_buffer
      - .actual_access:  read_only
        .address_space:  global
        .offset:         32
        .size:           8
        .value_kind:     global_buffer
      - .actual_access:  read_only
        .address_space:  global
        .offset:         40
        .size:           8
        .value_kind:     global_buffer
      - .actual_access:  read_only
        .address_space:  global
        .offset:         48
        .size:           8
        .value_kind:     global_buffer
      - .actual_access:  read_only
        .address_space:  global
        .offset:         56
        .size:           8
        .value_kind:     global_buffer
      - .actual_access:  read_only
        .address_space:  global
        .offset:         64
        .size:           8
        .value_kind:     global_buffer
      - .actual_access:  write_only
        .address_space:  global
        .offset:         72
        .size:           8
        .value_kind:     global_buffer
    .group_segment_fixed_size: 12800
    .kernarg_segment_align: 8
    .kernarg_segment_size: 80
    .language:       OpenCL C
    .language_version:
      - 2
      - 0
    .max_flat_workgroup_size: 256
    .name:           _Z12final_kernelPKfPKiPK15HIP_vector_typeIiLj4EES2_S2_S0_S0_S0_S0_Pf
    .private_segment_fixed_size: 0
    .sgpr_count:     50
    .sgpr_spill_count: 0
    .symbol:         _Z12final_kernelPKfPKiPK15HIP_vector_typeIiLj4EES2_S2_S0_S0_S0_S0_Pf.kd
    .uniform_work_group_size: 1
    .uses_dynamic_stack: false
    .vgpr_count:     140
    .vgpr_spill_count: 0
    .wavefront_size: 64
  - .agpr_count:     0
    .args:
      - .address_space:  global
        .offset:         0
        .size:           8
        .value_kind:     global_buffer
      - .address_space:  global
        .offset:         8
        .size:           8
        .value_kind:     global_buffer
      - .offset:         16
        .size:           4
        .value_kind:     by_value
      - .offset:         20
        .size:           4
        .value_kind:     by_value
      - .actual_access:  read_only
        .address_space:  global
        .offset:         24
        .size:           8
        .value_kind:     global_buffer
      - .offset:         32
        .size:           4
        .value_kind:     by_value
      - .actual_access:  read_only
        .address_space:  global
        .offset:         40
        .size:           8
        .value_kind:     global_buffer
      - .actual_access:  read_only
        .address_space:  global
        .offset:         48
        .size:           8
        .value_kind:     global_buffer
      - .actual_access:  write_only
        .address_space:  global
        .offset:         56
        .size:           8
        .value_kind:     global_buffer
      - .offset:         64
        .size:           4
        .value_kind:     by_value
      - .actual_access:  read_only
        .address_space:  global
        .offset:         72
        .size:           8
        .value_kind:     global_buffer
    .group_segment_fixed_size: 0
    .kernarg_segment_align: 8
    .kernarg_segment_size: 80
    .language:       OpenCL C
    .language_version:
      - 2
      - 0
    .max_flat_workgroup_size: 512
    .name:           _Z7gemm_x3ILi2ELi2ELi2ELi0EEvPKcS1_iiPKfiS3_PKiPciPy
    .private_segment_fixed_size: 0
    .sgpr_count:     38
    .sgpr_spill_count: 0
    .symbol:         _Z7gemm_x3ILi2ELi2ELi2ELi0EEvPKcS1_iiPKfiS3_PKiPciPy.kd
    .uniform_work_group_size: 1
    .uses_dynamic_stack: false
    .vgpr_count:     208
    .vgpr_spill_count: 0
    .wavefront_size: 64
  - .agpr_count:     0
    .args:
      - .address_space:  global
        .offset:         0
        .size:           8
        .value_kind:     global_buffer
      - .address_space:  global
        .offset:         8
        .size:           8
        .value_kind:     global_buffer
      - .offset:         16
        .size:           4
        .value_kind:     by_value
      - .offset:         20
        .size:           4
        .value_kind:     by_value
      - .actual_access:  read_only
        .address_space:  global
        .offset:         24
        .size:           8
        .value_kind:     global_buffer
      - .offset:         32
        .size:           4
        .value_kind:     by_value
      - .actual_access:  read_only
        .address_space:  global
        .offset:         40
        .size:           8
        .value_kind:     global_buffer
      - .actual_access:  read_only
        .address_space:  global
        .offset:         48
        .size:           8
        .value_kind:     global_buffer
      - .actual_access:  write_only
        .address_space:  global
        .offset:         56
        .size:           8
        .value_kind:     global_buffer
      - .offset:         64
        .size:           4
        .value_kind:     by_value
      - .actual_access:  read_only
        .address_space:  global
        .offset:         72
        .size:           8
        .value_kind:     global_buffer
    .group_segment_fixed_size: 0
    .kernarg_segment_align: 8
    .kernarg_segment_size: 80
    .language:       OpenCL C
    .language_version:
      - 2
      - 0
    .max_flat_workgroup_size: 512
    .name:           _Z7gemm_x3ILi2ELi2ELi1ELi1EEvPKcS1_iiPKfiS3_PKiPciPy
    .private_segment_fixed_size: 0
    .sgpr_count:     32
    .sgpr_spill_count: 0
    .symbol:         _Z7gemm_x3ILi2ELi2ELi1ELi1EEvPKcS1_iiPKfiS3_PKiPciPy.kd
    .uniform_work_group_size: 1
    .uses_dynamic_stack: false
    .vgpr_count:     114
    .vgpr_spill_count: 0
    .wavefront_size: 64
  - .agpr_count:     32
    .args:
      - .address_space:  global
        .offset:         0
        .size:           8
        .value_kind:     global_buffer
      - .address_space:  global
        .offset:         8
        .size:           8
        .value_kind:     global_buffer
      - .offset:         16
        .size:           4
        .value_kind:     by_value
      - .offset:         20
        .size:           4
        .value_kind:     by_value
      - .actual_access:  read_only
        .address_space:  global
        .offset:         24
        .size:           8
        .value_kind:     global_buffer
      - .offset:         32
        .size:           4
        .value_kind:     by_value
      - .actual_access:  read_only
        .address_space:  global
        .offset:         40
        .size:           8
        .value_kind:     global_buffer
      - .actual_access:  read_only
        .address_space:  global
        .offset:         48
        .size:           8
        .value_kind:     global_buffer
      - .actual_access:  write_only
        .address_space:  global
        .offset:         56
        .size:           8
        .value_kind:     global_buffer
      - .offset:         64
        .size:           4
        .value_kind:     by_value
      - .address_space:  global
        .offset:         72
        .size:           8
        .value_kind:     global_buffer
    .group_segment_fixed_size: 0
    .kernarg_segment_align: 8
    .kernarg_segment_size: 80
    .language:       OpenCL C
    .language_version:
      - 2
      - 0
    .max_flat_workgroup_size: 256
    .name:           _Z7gemm_x3ILi1ELi2ELi1ELi2EEvPKcS1_iiPKfiS3_PKiPciPy
    .private_segment_fixed_size: 0
    .sgpr_count:     29
    .sgpr_spill_count: 0
    .symbol:         _Z7gemm_x3ILi1ELi2ELi1ELi2EEvPKcS1_iiPKfiS3_PKiPciPy.kd
    .uniform_work_group_size: 1
    .uses_dynamic_stack: false
    .vgpr_count:     136
    .vgpr_spill_count: 0
    .wavefront_size: 64
  - .agpr_count:     0
    .args:
      - .actual_access:  read_only
        .address_space:  global
        .offset:         0
        .size:           8
        .value_kind:     global_buffer
      - .offset:         8
        .size:           4
        .value_kind:     by_value
      - .offset:         12
        .size:           4
        .value_kind:     by_value
      - .actual_access:  read_only
        .address_space:  global
        .offset:         16
        .size:           8
        .value_kind:     global_buffer
      - .offset:         24
        .size:           4
        .value_kind:     by_value
      - .offset:         28
        .size:           4
        .value_kind:     by_value
      - .actual_access:  read_only
        .address_space:  global
        .offset:         32
        .size:           8
        .value_kind:     global_buffer
      - .actual_access:  read_only
        .address_space:  global
        .offset:         40
        .size:           8
        .value_kind:     global_buffer
      - .actual_access:  read_only
        .address_space:  global
        .offset:         48
        .size:           8
        .value_kind:     global_buffer
      - .actual_access:  read_only
        .address_space:  global
        .offset:         56
        .size:           8
        .value_kind:     global_buffer
      - .actual_access:  write_only
        .address_space:  global
        .offset:         64
        .size:           8
        .value_kind:     global_buffer
      - .offset:         72
        .size:           4
        .value_kind:     by_value
      - .actual_access:  read_only
        .address_space:  global
        .offset:         80
        .size:           8
        .value_kind:     global_buffer
      - .offset:         88
        .size:           4
        .value_kind:     hidden_block_count_x
      - .offset:         92
        .size:           4
        .value_kind:     hidden_block_count_y
      - .offset:         96
        .size:           4
        .value_kind:     hidden_block_count_z
      - .offset:         100
        .size:           2
        .value_kind:     hidden_group_size_x
      - .offset:         102
        .size:           2
        .value_kind:     hidden_group_size_y
      - .offset:         104
        .size:           2
        .value_kind:     hidden_group_size_z
      - .offset:         106
        .size:           2
        .value_kind:     hidden_remainder_x
      - .offset:         108
        .size:           2
        .value_kind:     hidden_remainder_y
      - .offset:         110
        .size:           2
        .value_kind:     hidden_remainder_z
      - .offset:         128
        .size:           8
        .value_kind:     hidden_global_offset_x
      - .offset:         136
        .size:           8
        .value_kind:     hidden_global_offset_y
      - .offset:         144
        .size:           8
        .value_kind:     hidden_global_offset_z
      - .offset:         152
        .size:           2
        .value_kind:     hidden_grid_dims
    .group_segment_fixed_size: 16384
    .kernarg_segment_align: 8
    .kernarg_segment_size: 344
    .language:       OpenCL C
    .language_version:
      - 2
      - 0
    .max_flat_workgroup_size: 1024
    .name:           _Z13refine_kernelILi1ELi16ELi128ELb1ELi4EEvPKfiiS1_iiS1_PKiS3_S3_PfiPy
    .private_segment_fixed_size: 0
    .sgpr_count:     35
    .sgpr_spill_count: 0
    .symbol:         _Z13refine_kernelILi1ELi16ELi128ELb1ELi4EEvPKfiiS1_iiS1_PKiS3_S3_PfiPy.kd
    .uniform_work_group_size: 1
    .uses_dynamic_stack: false
    .vgpr_count:     64
    .vgpr_spill_count: 0
    .wavefront_size: 64
  - .agpr_count:     0
    .args:
      - .actual_access:  read_only
        .address_space:  global
        .offset:         0
        .size:           8
        .value_kind:     global_buffer
      - .offset:         8
        .size:           4
        .value_kind:     by_value
      - .offset:         12
        .size:           4
        .value_kind:     by_value
      - .actual_access:  read_only
        .address_space:  global
        .offset:         16
        .size:           8
        .value_kind:     global_buffer
      - .offset:         24
        .size:           4
        .value_kind:     by_value
      - .offset:         28
        .size:           4
        .value_kind:     by_value
      - .actual_access:  read_only
        .address_space:  global
        .offset:         32
        .size:           8
        .value_kind:     global_buffer
      - .actual_access:  read_only
        .address_space:  global
        .offset:         40
        .size:           8
        .value_kind:     global_buffer
      - .actual_access:  read_only
        .address_space:  global
        .offset:         48
        .size:           8
        .value_kind:     global_buffer
      - .actual_access:  read_only
        .address_space:  global
        .offset:         56
        .size:           8
        .value_kind:     global_buffer
      - .actual_access:  write_only
        .address_space:  global
        .offset:         64
        .size:           8
        .value_kind:     global_buffer
      - .offset:         72
        .size:           4
        .value_kind:     by_value
      - .actual_access:  read_only
        .address_space:  global
        .offset:         80
        .size:           8
        .value_kind:     global_buffer
      - .offset:         88
        .size:           4
        .value_kind:     hidden_block_count_x
      - .offset:         92
        .size:           4
        .value_kind:     hidden_block_count_y
      - .offset:         96
        .size:           4
        .value_kind:     hidden_block_count_z
      - .offset:         100
        .size:           2
        .value_kind:     hidden_group_size_x
      - .offset:         102
        .size:           2
        .value_kind:     hidden_group_size_y
      - .offset:         104
        .size:           2
        .value_kind:     hidden_group_size_z
      - .offset:         106
        .size:           2
        .value_kind:     hidden_remainder_x
      - .offset:         108
        .size:           2
        .value_kind:     hidden_remainder_y
      - .offset:         110
        .size:           2
        .value_kind:     hidden_remainder_z
      - .offset:         128
        .size:           8
        .value_kind:     hidden_global_offset_x
      - .offset:         136
        .size:           8
        .value_kind:     hidden_global_offset_y
      - .offset:         144
        .size:           8
        .value_kind:     hidden_global_offset_z
      - .offset:         152
        .size:           2
        .value_kind:     hidden_grid_dims
    .group_segment_fixed_size: 16384
    .kernarg_segment_align: 8
    .kernarg_segment_size: 344
    .language:       OpenCL C
    .language_version:
      - 2
      - 0
    .max_flat_workgroup_size: 1024
    .name:           _Z13refine_kernelILi2ELi16ELi64ELb0ELi4EEvPKfiiS1_iiS1_PKiS3_S3_PfiPy
    .private_segment_fixed_size: 0
    .sgpr_count:     35
    .sgpr_spill_count: 0
    .symbol:         _Z13refine_kernelILi2ELi16ELi64ELb0ELi4EEvPKfiiS1_iiS1_PKiS3_S3_PfiPy.kd
    .uniform_work_group_size: 1
    .uses_dynamic_stack: false
    .vgpr_count:     85
    .vgpr_spill_count: 0
    .wavefront_size: 64
  - .agpr_count:     0
    .args:
      - .actual_access:  read_only
        .address_space:  global
        .offset:         0
        .size:           8
        .value_kind:     global_buffer
      - .offset:         8
        .size:           4
        .value_kind:     by_value
      - .offset:         12
        .size:           4
        .value_kind:     by_value
      - .actual_access:  read_only
        .address_space:  global
        .offset:         16
        .size:           8
        .value_kind:     global_buffer
      - .offset:         24
        .size:           4
        .value_kind:     by_value
      - .offset:         28
        .size:           4
        .value_kind:     by_value
      - .actual_access:  read_only
        .address_space:  global
        .offset:         32
        .size:           8
        .value_kind:     global_buffer
      - .actual_access:  read_only
        .address_space:  global
        .offset:         40
        .size:           8
        .value_kind:     global_buffer
      - .actual_access:  read_only
        .address_space:  global
        .offset:         48
        .size:           8
        .value_kind:     global_buffer
      - .actual_access:  read_only
        .address_space:  global
        .offset:         56
        .size:           8
        .value_kind:     global_buffer
      - .actual_access:  read_only
        .address_space:  global
        .offset:         64
        .size:           8
        .value_kind:     global_buffer
      - .offset:         72
        .size:           4
        .value_kind:     by_value
      - .address_space:  global
        .offset:         80
        .size:           8
        .value_kind:     global_buffer
      - .offset:         88
        .size:           4
        .value_kind:     hidden_block_count_x
      - .offset:         92
        .size:           4
        .value_kind:     hidden_block_count_y
      - .offset:         96
        .size:           4
        .value_kind:     hidden_block_count_z
      - .offset:         100
        .size:           2
        .value_kind:     hidden_group_size_x
      - .offset:         102
        .size:           2
        .value_kind:     hidden_group_size_y
      - .offset:         104
        .size:           2
        .value_kind:     hidden_group_size_z
      - .offset:         106
        .size:           2
        .value_kind:     hidden_remainder_x
      - .offset:         108
        .size:           2
        .value_kind:     hidden_remainder_y
      - .offset:         110
        .size:           2
        .value_kind:     hidden_remainder_z
      - .offset:         128
        .size:           8
        .value_kind:     hidden_global_offset_x
      - .offset:         136
        .size:           8
        .value_kind:     hidden_global_offset_y
      - .offset:         144
        .size:           8
        .value_kind:     hidden_global_offset_z
      - .offset:         152
        .size:           2
        .value_kind:     hidden_grid_dims
    .group_segment_fixed_size: 8192
    .kernarg_segment_align: 8
    .kernarg_segment_size: 344
    .language:       OpenCL C
    .language_version:
      - 2
      - 0
    .max_flat_workgroup_size: 512
    .name:           _Z13refine_kernelILi3ELi8ELi64ELb0ELi4EEvPKfiiS1_iiS1_PKiS3_S3_PfiPy
    .private_segment_fixed_size: 0
    .sgpr_count:     38
    .sgpr_spill_count: 0
    .symbol:         _Z13refine_kernelILi3ELi8ELi64ELb0ELi4EEvPKfiiS1_iiS1_PKiS3_S3_PfiPy.kd
    .uniform_work_group_size: 1
    .uses_dynamic_stack: false
    .vgpr_count:     88
    .vgpr_spill_count: 0
    .wavefront_size: 64
